# v9 plus ticket-atomic fix, plus MoE gate/up K-loop: four of the six LDS-DMA issues of each SP2 load segment deferred into the following MFMA segment (saddr forms, recounted vmcnt)
# speedup vs baseline: 1.0031x; 1.0031x over previous
.LBB0_820:
	v_xor_b32_e32 v218, 16, v231
	v_and_b32_e32 v216, 64, v231
	v_add_u32_e32 v216, 64, v216
	v_xor_b32_e32 v217, 32, v231
	v_cmp_lt_i32_e32 vcc, v218, v216
	v_mov_b32_e32 v142, 0xbfb8aa3b
	v_mov_b32_e32 v143, 1.0
	v_cndmask_b32_e32 v218, v231, v218, vcc
	v_cmp_lt_i32_e32 vcc, v217, v216
	v_lshlrev_b32_e32 v218, 2, v218
	v_mov_b32_e32 v144, 0x41000000
	v_cndmask_b32_e32 v217, v231, v217, vcc
	v_lshlrev_b32_e32 v217, 2, v217
	ds_bpermute_b32 v156, v218, v244
	ds_bpermute_b32 v157, v218, v245
	ds_bpermute_b32 v158, v218, v246
	ds_bpermute_b32 v159, v218, v247
	ds_bpermute_b32 v160, v218, v248
	ds_bpermute_b32 v161, v218, v249
	ds_bpermute_b32 v162, v218, v250
	ds_bpermute_b32 v163, v218, v251
	v_lshl_add_u32 v221, s52, 8, v149
	v_lshl_or_b32 v220, s63, 7, v153
	v_mad_u32_u24 v219, v221, s33, v220
	s_waitcnt lgkmcnt(7)
	v_add_f32_e32 v244, v244, v156
	ds_bpermute_b32 v156, v217, v244
	s_waitcnt lgkmcnt(7)
	v_add_f32_e32 v245, v245, v157
	ds_bpermute_b32 v157, v217, v245
	s_waitcnt lgkmcnt(7)
	v_add_f32_e32 v246, v246, v158
	ds_bpermute_b32 v158, v217, v246
	s_waitcnt lgkmcnt(7)
	v_add_f32_e32 v247, v247, v159
	ds_bpermute_b32 v159, v217, v247
	s_waitcnt lgkmcnt(7)
	v_add_f32_e32 v248, v248, v160
	ds_bpermute_b32 v160, v217, v248
	s_waitcnt lgkmcnt(7)
	v_add_f32_e32 v249, v249, v161
	ds_bpermute_b32 v161, v217, v249
	s_waitcnt lgkmcnt(7)
	v_add_f32_e32 v250, v250, v162
	ds_bpermute_b32 v162, v217, v250
	s_waitcnt lgkmcnt(7)
	v_add_f32_e32 v251, v251, v163
	ds_bpermute_b32 v163, v217, v251
	s_waitcnt lgkmcnt(7)
	v_add_f32_e32 v244, v244, v156
	v_fmamk_f32 v244, v244, 0x3a800000, v224
	s_waitcnt lgkmcnt(6)
	v_add_f32_e32 v245, v245, v157
	v_fmamk_f32 v245, v245, 0x3a800000, v224
	s_waitcnt lgkmcnt(5)
	v_add_f32_e32 v246, v246, v158
	v_fmamk_f32 v246, v246, 0x3a800000, v224
	s_waitcnt lgkmcnt(4)
	v_add_f32_e32 v247, v247, v159
	v_fmamk_f32 v247, v247, 0x3a800000, v224
	s_waitcnt lgkmcnt(3)
	v_add_f32_e32 v248, v248, v160
	v_fmamk_f32 v248, v248, 0x3a800000, v224
	s_waitcnt lgkmcnt(2)
	v_add_f32_e32 v249, v249, v161
	v_fmamk_f32 v249, v249, 0x3a800000, v224
	s_waitcnt lgkmcnt(1)
	v_add_f32_e32 v250, v250, v162
	v_fmamk_f32 v250, v250, 0x3a800000, v224
	s_waitcnt lgkmcnt(0)
	v_add_f32_e32 v251, v251, v163
	v_fmamk_f32 v251, v251, 0x3a800000, v224
	v_rsq_f32_e32 v244, v244
	v_rsq_f32_e32 v245, v245
	v_rsq_f32_e32 v246, v246
	v_rsq_f32_e32 v247, v247
	v_rsq_f32_e32 v248, v248
	v_rsq_f32_e32 v249, v249
	v_rsq_f32_e32 v250, v250
	v_rsq_f32_e32 v251, v251
	v_pk_mul_f32 v[156:157], v[126:127], v[244:245] op_sel_hi:[1,0]
	v_pk_mul_f32 v[158:159], v[128:129], v[244:245] op_sel_hi:[1,0]
	v_pk_mul_f32 v[160:161], v[118:119], v[244:245] op_sel_hi:[1,0]
	v_pk_mul_f32 v[162:163], v[156:157], v[142:143] op_sel_hi:[1,0]
	v_pk_mul_f32 v[170:171], v[158:159], v[142:143] op_sel_hi:[1,0]
	v_pk_mul_f32 v[172:173], v[160:161], v[142:143] op_sel_hi:[1,0]
	v_exp_f32_e32 v162, v162
	v_pk_mul_f32 v[174:175], v[120:121], v[244:245] op_sel_hi:[1,0]
	v_exp_f32_e32 v170, v170
	v_pk_mul_f32 v[176:177], v[110:111], v[244:245] op_sel:[0,1] op_sel_hi:[1,1]
	v_exp_f32_e32 v172, v172
	v_pk_mul_f32 v[178:179], v[174:175], v[142:143] op_sel_hi:[1,0]
	v_pk_mul_f32 v[180:181], v[176:177], v[142:143] op_sel_hi:[1,0]
	v_pk_mul_f32 v[182:183], v[112:113], v[244:245] op_sel:[0,1] op_sel_hi:[1,1]
	v_exp_f32_e32 v178, v178
	v_pk_mul_f32 v[184:185], v[102:103], v[244:245] op_sel:[0,1] op_sel_hi:[1,1]
	v_exp_f32_e32 v163, v163
	v_pk_mul_f32 v[186:187], v[182:183], v[142:143] op_sel_hi:[1,0]
	v_exp_f32_e32 v171, v171
	v_pk_mul_f32 v[188:189], v[184:185], v[142:143] op_sel_hi:[1,0]
	v_exp_f32_e32 v173, v173
	v_pk_mul_f32 v[190:191], v[104:105], v[244:245] op_sel:[0,1] op_sel_hi:[1,1]
	v_exp_f32_e32 v179, v179
	v_pk_mul_f32 v[192:193], v[122:123], v[244:245] op_sel_hi:[1,0]
	v_pk_add_f32 v[162:163], v[162:163], v[142:143] op_sel:[0,1] op_sel_hi:[1,1]
	v_exp_f32_e32 v180, v180
	v_pk_add_f32 v[170:171], v[170:171], v[142:143] op_sel:[0,1] op_sel_hi:[1,1]
	v_rcp_f32_e32 v162, v162
	v_pk_add_f32 v[172:173], v[172:173], v[142:143] op_sel:[0,1] op_sel_hi:[1,1]
	v_rcp_f32_e32 v170, v170
	v_pk_add_f32 v[178:179], v[178:179], v[142:143] op_sel:[0,1] op_sel_hi:[1,1]
	v_rcp_f32_e32 v172, v172
	v_pk_mul_f32 v[194:195], v[190:191], v[142:143] op_sel_hi:[1,0]
	v_rcp_f32_e32 v178, v178
	v_pk_mul_f32 v[192:193], v[192:193], v[156:157]
	v_exp_f32_e32 v186, v186
	v_pk_mul_f32 v[156:157], v[124:125], v[244:245] op_sel_hi:[1,0]
	v_exp_f32_e32 v188, v188
	v_pk_mul_f32 v[196:197], v[114:115], v[244:245] op_sel_hi:[1,0]
	v_rcp_f32_e32 v163, v163
	v_pk_mul_f32 v[198:199], v[94:95], v[246:247] op_sel_hi:[1,0]
	v_exp_f32_e32 v194, v194
	v_pk_mul_f32 v[156:157], v[156:157], v[158:159]
	v_rcp_f32_e32 v171, v171
	v_pk_mul_f32 v[196:197], v[196:197], v[160:161]
	v_rcp_f32_e32 v173, v173
	v_pk_mul_f32 v[158:159], v[116:117], v[244:245] op_sel_hi:[1,0]
	v_exp_f32_e32 v181, v181
	v_pk_mul_f32 v[192:193], v[192:193], v[162:163]
	v_rcp_f32_e32 v179, v179
	v_pk_mul_f32 v[160:161], v[198:199], v[142:143] op_sel_hi:[1,0]
	v_exp_f32_e32 v187, v187
	v_pk_mul_f32 v[192:193], v[192:193], v[144:145] op_sel_hi:[1,0]
	v_exp_f32_e32 v189, v189
	v_pk_mul_f32 v[156:157], v[156:157], v[170:171]
	v_exp_f32_e32 v195, v195
	v_pk_mul_f32 v[196:197], v[196:197], v[172:173]
	v_pk_add_f32 v[180:181], v[180:181], v[142:143] op_sel:[0,1] op_sel_hi:[1,1]
	v_med3_f32 v192, v192, s87, v227
	v_pk_mul_f32 v[156:157], v[156:157], v[144:145] op_sel_hi:[1,0]
	v_pk_mul_f32 v[196:197], v[196:197], v[144:145] op_sel_hi:[1,0]
	v_rcp_f32_e32 v180, v180
	v_pk_add_f32 v[186:187], v[186:187], v[142:143] op_sel:[0,1] op_sel_hi:[1,1]
	v_pk_add_f32 v[188:189], v[188:189], v[142:143] op_sel:[0,1] op_sel_hi:[1,1]
	v_pk_mul_f32 v[162:163], v[96:97], v[246:247] op_sel_hi:[1,0]
	v_pk_mul_f32 v[170:171], v[86:87], v[246:247] op_sel_hi:[1,0]
	v_med3_f32 v193, v193, s87, v227
	v_med3_f32 v156, v156, s87, v227
	v_med3_f32 v196, v196, s87, v227
	v_pk_mul_f32 v[158:159], v[158:159], v[174:175]
	v_rcp_f32_e32 v186, v186
	v_pk_add_f32 v[194:195], v[194:195], v[142:143] op_sel:[0,1] op_sel_hi:[1,1]
	v_pk_mul_f32 v[158:159], v[158:159], v[178:179]
	v_rcp_f32_e32 v188, v188
	v_pk_mul_f32 v[172:173], v[162:163], v[142:143] op_sel_hi:[1,0]
	v_pk_mul_f32 v[158:159], v[158:159], v[144:145] op_sel_hi:[1,0]
	v_exp_f32_e32 v160, v160
	v_pk_mul_f32 v[174:175], v[170:171], v[142:143] op_sel_hi:[1,0]
	v_pk_mul_f32 v[178:179], v[88:89], v[246:247] op_sel_hi:[1,0]
	v_cvt_pk_fp8_f32 v192, v192, v193
	v_med3_f32 v157, v157, s87, v227
	v_med3_f32 v197, v197, s87, v227
	v_med3_f32 v158, v158, s87, v227
	v_rcp_f32_e32 v194, v194
	v_pk_mul_f32 v[200:201], v[178:179], v[142:143] op_sel_hi:[1,0]
	v_exp_f32_e32 v172, v172
	v_cvt_pk_fp8_f32 v192, v156, v157 op_sel:[0,0,1]
	v_exp_f32_e32 v174, v174
	v_cvt_pk_fp8_f32 v193, v196, v197
	v_rcp_f32_e32 v181, v181
	v_med3_f32 v159, v159, s87, v227
	v_exp_f32_e32 v200, v200
	v_pk_mul_f32 v[156:157], v[106:107], v[244:245] op_sel:[0,1] op_sel_hi:[1,1]
	v_rcp_f32_e32 v187, v187
	v_cvt_pk_fp8_f32 v193, v158, v159 op_sel:[0,0,1]
	v_rcp_f32_e32 v189, v189
	v_pk_mul_f32 v[156:157], v[156:157], v[176:177]
	v_exp_f32_e32 v161, v161
	global_store_dwordx2 v219, v[192:193], s[26:27]
	v_rcp_f32_e32 v195, v195
	v_pk_mul_f32 v[156:157], v[156:157], v[180:181]
	v_exp_f32_e32 v173, v173
	v_pk_mul_f32 v[158:159], v[108:109], v[244:245] op_sel:[0,1] op_sel_hi:[1,1]
	v_exp_f32_e32 v175, v175
	v_pk_mul_f32 v[156:157], v[156:157], v[144:145] op_sel_hi:[1,0]
	v_exp_f32_e32 v201, v201
	v_pk_mul_f32 v[176:177], v[98:99], v[244:245] op_sel:[0,1] op_sel_hi:[1,1]
	v_pk_add_f32 v[160:161], v[160:161], v[142:143] op_sel:[0,1] op_sel_hi:[1,1]
	v_pk_mul_f32 v[180:181], v[78:79], v[246:247] op_sel:[0,1] op_sel_hi:[1,1]
	v_med3_f32 v156, v156, s87, v227
	v_pk_mul_f32 v[158:159], v[158:159], v[182:183]
	v_pk_mul_f32 v[176:177], v[176:177], v[184:185]
	v_pk_mul_f32 v[182:183], v[100:101], v[244:245] op_sel:[0,1] op_sel_hi:[1,1]
	v_pk_mul_f32 v[158:159], v[158:159], v[186:187]
	v_pk_mul_f32 v[176:177], v[176:177], v[188:189]
	v_rcp_f32_e32 v160, v160
	v_pk_mul_f32 v[158:159], v[158:159], v[144:145] op_sel_hi:[1,0]
	v_pk_mul_f32 v[176:177], v[176:177], v[144:145] op_sel_hi:[1,0]
	v_pk_add_f32 v[172:173], v[172:173], v[142:143] op_sel:[0,1] op_sel_hi:[1,1]
	v_pk_add_f32 v[174:175], v[174:175], v[142:143] op_sel:[0,1] op_sel_hi:[1,1]
	v_pk_mul_f32 v[184:185], v[180:181], v[142:143] op_sel_hi:[1,0]
	v_pk_mul_f32 v[186:187], v[80:81], v[246:247] op_sel:[0,1] op_sel_hi:[1,1]
	v_pk_mul_f32 v[188:189], v[70:71], v[246:247] op_sel:[0,1] op_sel_hi:[1,1]
	v_med3_f32 v157, v157, s87, v227
	v_med3_f32 v158, v158, s87, v227
	v_med3_f32 v176, v176, s87, v227
	v_pk_mul_f32 v[182:183], v[182:183], v[190:191]
	v_rcp_f32_e32 v172, v172
	v_pk_add_f32 v[200:201], v[200:201], v[142:143] op_sel:[0,1] op_sel_hi:[1,1]
	v_pk_mul_f32 v[182:183], v[182:183], v[194:195]
	v_rcp_f32_e32 v174, v174
	v_pk_mul_f32 v[190:191], v[186:187], v[142:143] op_sel_hi:[1,0]
	v_pk_mul_f32 v[182:183], v[182:183], v[144:145] op_sel_hi:[1,0]
	v_exp_f32_e32 v184, v184
	v_pk_mul_f32 v[192:193], v[188:189], v[142:143] op_sel_hi:[1,0]
	v_pk_mul_f32 v[194:195], v[72:73], v[246:247] op_sel:[0,1] op_sel_hi:[1,1]
	v_cvt_pk_fp8_f32 v156, v156, v157
	v_med3_f32 v159, v159, s87, v227
	v_med3_f32 v177, v177, s87, v227
	v_med3_f32 v182, v182, s87, v227
	v_rcp_f32_e32 v200, v200
	v_pk_mul_f32 v[196:197], v[194:195], v[142:143] op_sel_hi:[1,0]
	v_exp_f32_e32 v190, v190
	v_cvt_pk_fp8_f32 v156, v158, v159 op_sel:[0,0,1]
	v_exp_f32_e32 v192, v192
	v_cvt_pk_fp8_f32 v157, v176, v177
	v_rcp_f32_e32 v161, v161
	v_med3_f32 v183, v183, s87, v227
	v_exp_f32_e32 v196, v196
	v_pk_mul_f32 v[158:159], v[90:91], v[246:247] op_sel_hi:[1,0]
	v_rcp_f32_e32 v173, v173
	v_cvt_pk_fp8_f32 v157, v182, v183 op_sel:[0,0,1]
	v_rcp_f32_e32 v175, v175
	v_pk_mul_f32 v[158:159], v[158:159], v[198:199]
	v_exp_f32_e32 v185, v185
	v_pk_mul_f32 v[176:177], v[92:93], v[246:247] op_sel_hi:[1,0]
	v_rcp_f32_e32 v201, v201
	v_pk_mul_f32 v[158:159], v[158:159], v[160:161]
	v_exp_f32_e32 v191, v191
	v_pk_mul_f32 v[160:161], v[82:83], v[246:247] op_sel_hi:[1,0]
	v_exp_f32_e32 v193, v193
	v_pk_mul_f32 v[158:159], v[158:159], v[144:145] op_sel_hi:[1,0]
	v_exp_f32_e32 v197, v197
	v_pk_add_f32 v[184:185], v[184:185], v[142:143] op_sel:[0,1] op_sel_hi:[1,1]
	v_pk_mul_f32 v[182:183], v[62:63], v[248:249] op_sel_hi:[1,0]
	v_med3_f32 v158, v158, s87, v227
	v_pk_mul_f32 v[176:177], v[176:177], v[162:163]
	v_pk_mul_f32 v[160:161], v[160:161], v[170:171]
	v_pk_mul_f32 v[162:163], v[84:85], v[246:247] op_sel_hi:[1,0]
	v_pk_mul_f32 v[176:177], v[176:177], v[172:173]
	v_pk_mul_f32 v[160:161], v[160:161], v[174:175]
	v_rcp_f32_e32 v184, v184
	v_pk_mul_f32 v[176:177], v[176:177], v[144:145] op_sel_hi:[1,0]
	v_pk_mul_f32 v[160:161], v[160:161], v[144:145] op_sel_hi:[1,0]
	v_pk_add_f32 v[190:191], v[190:191], v[142:143] op_sel:[0,1] op_sel_hi:[1,1]
	v_pk_add_f32 v[192:193], v[192:193], v[142:143] op_sel:[0,1] op_sel_hi:[1,1]
	v_pk_mul_f32 v[170:171], v[182:183], v[142:143] op_sel_hi:[1,0]
	v_pk_mul_f32 v[172:173], v[64:65], v[248:249] op_sel_hi:[1,0]
	v_pk_mul_f32 v[174:175], v[54:55], v[248:249] op_sel_hi:[1,0]
	v_med3_f32 v159, v159, s87, v227
	v_med3_f32 v176, v176, s87, v227
	v_med3_f32 v160, v160, s87, v227
	v_pk_mul_f32 v[162:163], v[162:163], v[178:179]
	v_rcp_f32_e32 v190, v190
	v_pk_add_f32 v[196:197], v[196:197], v[142:143] op_sel:[0,1] op_sel_hi:[1,1]
	v_pk_mul_f32 v[162:163], v[162:163], v[200:201]
	v_rcp_f32_e32 v192, v192
	v_pk_mul_f32 v[178:179], v[172:173], v[142:143] op_sel_hi:[1,0]
	v_pk_mul_f32 v[162:163], v[162:163], v[144:145] op_sel_hi:[1,0]
	v_exp_f32_e32 v170, v170
	v_pk_mul_f32 v[198:199], v[174:175], v[142:143] op_sel_hi:[1,0]
	v_pk_mul_f32 v[200:201], v[56:57], v[248:249] op_sel_hi:[1,0]
	v_cvt_pk_fp8_f32 v158, v158, v159
	v_med3_f32 v177, v177, s87, v227
	v_med3_f32 v161, v161, s87, v227
	v_med3_f32 v162, v162, s87, v227
	v_rcp_f32_e32 v196, v196
	v_pk_mul_f32 v[202:203], v[200:201], v[142:143] op_sel_hi:[1,0]
	v_exp_f32_e32 v178, v178
	v_cvt_pk_fp8_f32 v158, v176, v177 op_sel:[0,0,1]
	v_exp_f32_e32 v198, v198
	v_cvt_pk_fp8_f32 v159, v160, v161
	v_rcp_f32_e32 v185, v185
	v_med3_f32 v163, v163, s87, v227
	v_exp_f32_e32 v202, v202
	v_add_u32_e32 v160, 0xe000, v219
	v_rcp_f32_e32 v191, v191
	v_cvt_pk_fp8_f32 v159, v162, v163 op_sel:[0,0,1]
	global_store_dwordx2 v160, v[156:157], s[26:27]
	v_rcp_f32_e32 v193, v193
	v_pk_mul_f32 v[156:157], v[74:75], v[246:247] op_sel:[0,1] op_sel_hi:[1,1]
	v_exp_f32_e32 v171, v171
	v_pk_mul_f32 v[160:161], v[76:77], v[246:247] op_sel:[0,1] op_sel_hi:[1,1]
	v_rcp_f32_e32 v197, v197
	v_pk_mul_f32 v[156:157], v[156:157], v[180:181]
	v_exp_f32_e32 v179, v179
	v_pk_mul_f32 v[162:163], v[66:67], v[246:247] op_sel:[0,1] op_sel_hi:[1,1]
	v_exp_f32_e32 v199, v199
	v_pk_mul_f32 v[156:157], v[156:157], v[184:185]
	v_exp_f32_e32 v203, v203
	v_pk_add_f32 v[170:171], v[170:171], v[142:143] op_sel:[0,1] op_sel_hi:[1,1]
	v_pk_mul_f32 v[156:157], v[156:157], v[144:145] op_sel_hi:[1,0]
	v_pk_mul_f32 v[176:177], v[46:47], v[248:249] op_sel:[0,1] op_sel_hi:[1,1]
	v_pk_mul_f32 v[160:161], v[160:161], v[186:187]
	v_med3_f32 v156, v156, s87, v227
	v_pk_mul_f32 v[162:163], v[162:163], v[188:189]
	v_pk_mul_f32 v[160:161], v[160:161], v[190:191]
	v_pk_mul_f32 v[180:181], v[68:69], v[246:247] op_sel:[0,1] op_sel_hi:[1,1]
	v_pk_mul_f32 v[162:163], v[162:163], v[192:193]
	v_pk_mul_f32 v[160:161], v[160:161], v[144:145] op_sel_hi:[1,0]
	v_rcp_f32_e32 v170, v170
	v_pk_mul_f32 v[162:163], v[162:163], v[144:145] op_sel_hi:[1,0]
	v_pk_add_f32 v[178:179], v[178:179], v[142:143] op_sel:[0,1] op_sel_hi:[1,1]
	v_pk_add_f32 v[198:199], v[198:199], v[142:143] op_sel:[0,1] op_sel_hi:[1,1]
	v_pk_mul_f32 v[184:185], v[176:177], v[142:143] op_sel_hi:[1,0]
	v_pk_mul_f32 v[186:187], v[48:49], v[248:249] op_sel:[0,1] op_sel_hi:[1,1]
	v_pk_mul_f32 v[188:189], v[38:39], v[248:249] op_sel:[0,1] op_sel_hi:[1,1]
	v_med3_f32 v157, v157, s87, v227
	v_med3_f32 v160, v160, s87, v227
	v_med3_f32 v162, v162, s87, v227
	v_pk_mul_f32 v[180:181], v[180:181], v[194:195]
	v_rcp_f32_e32 v178, v178
	v_pk_add_f32 v[202:203], v[202:203], v[142:143] op_sel:[0,1] op_sel_hi:[1,1]
	v_pk_mul_f32 v[180:181], v[180:181], v[196:197]
	v_rcp_f32_e32 v198, v198
	v_pk_mul_f32 v[190:191], v[186:187], v[142:143] op_sel_hi:[1,0]
	v_pk_mul_f32 v[180:181], v[180:181], v[144:145] op_sel_hi:[1,0]
	v_exp_f32_e32 v184, v184
	v_pk_mul_f32 v[192:193], v[188:189], v[142:143] op_sel_hi:[1,0]
	v_pk_mul_f32 v[194:195], v[40:41], v[248:249] op_sel:[0,1] op_sel_hi:[1,1]
	v_cvt_pk_fp8_f32 v156, v156, v157
	v_med3_f32 v161, v161, s87, v227
	v_med3_f32 v163, v163, s87, v227
	v_med3_f32 v180, v180, s87, v227
	v_rcp_f32_e32 v202, v202
	v_pk_mul_f32 v[196:197], v[194:195], v[142:143] op_sel_hi:[1,0]
	v_exp_f32_e32 v190, v190
	v_cvt_pk_fp8_f32 v156, v160, v161 op_sel:[0,0,1]
	v_exp_f32_e32 v192, v192
	v_cvt_pk_fp8_f32 v157, v162, v163
	v_rcp_f32_e32 v171, v171
	v_med3_f32 v181, v181, s87, v227
	v_exp_f32_e32 v196, v196
	v_add_u32_e32 v160, 0x1c000, v219
	v_rcp_f32_e32 v179, v179
	v_cvt_pk_fp8_f32 v157, v180, v181 op_sel:[0,0,1]
	global_store_dwordx2 v160, v[158:159], s[26:27]
	v_rcp_f32_e32 v199, v199
	v_pk_mul_f32 v[158:159], v[58:59], v[248:249] op_sel_hi:[1,0]
	v_exp_f32_e32 v185, v185
	v_pk_mul_f32 v[160:161], v[60:61], v[248:249] op_sel_hi:[1,0]
	v_rcp_f32_e32 v203, v203
	v_pk_mul_f32 v[158:159], v[158:159], v[182:183]
	v_exp_f32_e32 v191, v191
	v_pk_mul_f32 v[162:163], v[50:51], v[248:249] op_sel_hi:[1,0]
	v_exp_f32_e32 v193, v193
	v_pk_mul_f32 v[158:159], v[158:159], v[170:171]
	v_exp_f32_e32 v197, v197
	v_pk_add_f32 v[184:185], v[184:185], v[142:143] op_sel:[0,1] op_sel_hi:[1,1]
	v_pk_mul_f32 v[158:159], v[158:159], v[144:145] op_sel_hi:[1,0]
	v_pk_mul_f32 v[170:171], v[30:31], v[250:251] op_sel_hi:[1,0]
	v_pk_mul_f32 v[160:161], v[160:161], v[172:173]
	v_med3_f32 v158, v158, s87, v227
	v_pk_mul_f32 v[162:163], v[162:163], v[174:175]
	v_pk_mul_f32 v[160:161], v[160:161], v[178:179]
	v_pk_mul_f32 v[172:173], v[52:53], v[248:249] op_sel_hi:[1,0]
	v_pk_mul_f32 v[162:163], v[162:163], v[198:199]
	v_pk_mul_f32 v[160:161], v[160:161], v[144:145] op_sel_hi:[1,0]
	v_rcp_f32_e32 v184, v184
	v_pk_mul_f32 v[162:163], v[162:163], v[144:145] op_sel_hi:[1,0]
	v_pk_add_f32 v[190:191], v[190:191], v[142:143] op_sel:[0,1] op_sel_hi:[1,1]
	v_pk_add_f32 v[192:193], v[192:193], v[142:143] op_sel:[0,1] op_sel_hi:[1,1]
	v_pk_mul_f32 v[174:175], v[170:171], v[142:143] op_sel_hi:[1,0]
	v_pk_mul_f32 v[178:179], v[32:33], v[250:251] op_sel_hi:[1,0]
	v_pk_mul_f32 v[180:181], v[22:23], v[250:251] op_sel_hi:[1,0]
	v_med3_f32 v159, v159, s87, v227
	v_med3_f32 v160, v160, s87, v227
	v_med3_f32 v162, v162, s87, v227
	v_pk_mul_f32 v[172:173], v[172:173], v[200:201]
	v_rcp_f32_e32 v190, v190
	v_pk_add_f32 v[196:197], v[196:197], v[142:143] op_sel:[0,1] op_sel_hi:[1,1]
	v_pk_mul_f32 v[172:173], v[172:173], v[202:203]
	v_rcp_f32_e32 v192, v192
	v_pk_mul_f32 v[182:183], v[178:179], v[142:143] op_sel_hi:[1,0]
	v_pk_mul_f32 v[172:173], v[172:173], v[144:145] op_sel_hi:[1,0]
	v_exp_f32_e32 v174, v174
	v_pk_mul_f32 v[198:199], v[180:181], v[142:143] op_sel_hi:[1,0]
	v_pk_mul_f32 v[200:201], v[24:25], v[250:251] op_sel_hi:[1,0]
	v_cvt_pk_fp8_f32 v158, v158, v159
	v_med3_f32 v161, v161, s87, v227
	v_med3_f32 v163, v163, s87, v227
	v_med3_f32 v172, v172, s87, v227
	v_rcp_f32_e32 v196, v196
	v_pk_mul_f32 v[202:203], v[200:201], v[142:143] op_sel_hi:[1,0]
	v_exp_f32_e32 v182, v182
	v_cvt_pk_fp8_f32 v158, v160, v161 op_sel:[0,0,1]
	v_exp_f32_e32 v198, v198
	v_cvt_pk_fp8_f32 v159, v162, v163
	v_rcp_f32_e32 v185, v185
	v_med3_f32 v173, v173, s87, v227
	v_exp_f32_e32 v202, v202
	v_add_u32_e32 v160, 0x2a000, v219
	v_rcp_f32_e32 v191, v191
	v_cvt_pk_fp8_f32 v159, v172, v173 op_sel:[0,0,1]
	global_store_dwordx2 v160, v[156:157], s[26:27]
	v_rcp_f32_e32 v193, v193
	v_pk_mul_f32 v[156:157], v[42:43], v[248:249] op_sel:[0,1] op_sel_hi:[1,1]
	v_exp_f32_e32 v175, v175
	v_pk_mul_f32 v[160:161], v[44:45], v[248:249] op_sel:[0,1] op_sel_hi:[1,1]
	v_rcp_f32_e32 v197, v197
	v_pk_mul_f32 v[156:157], v[156:157], v[176:177]
	v_exp_f32_e32 v183, v183
	v_pk_mul_f32 v[162:163], v[34:35], v[248:249] op_sel:[0,1] op_sel_hi:[1,1]
	v_exp_f32_e32 v199, v199
	v_pk_mul_f32 v[156:157], v[156:157], v[184:185]
	v_exp_f32_e32 v203, v203
	v_pk_add_f32 v[174:175], v[174:175], v[142:143] op_sel:[0,1] op_sel_hi:[1,1]
	v_pk_mul_f32 v[156:157], v[156:157], v[144:145] op_sel_hi:[1,0]
	v_pk_mul_f32 v[172:173], v[14:15], v[250:251] op_sel:[0,1] op_sel_hi:[1,1]
	v_pk_mul_f32 v[160:161], v[160:161], v[186:187]
	v_med3_f32 v156, v156, s87, v227
	v_pk_mul_f32 v[162:163], v[162:163], v[188:189]
	v_pk_mul_f32 v[160:161], v[160:161], v[190:191]
	v_pk_mul_f32 v[176:177], v[36:37], v[248:249] op_sel:[0,1] op_sel_hi:[1,1]
	v_pk_mul_f32 v[162:163], v[162:163], v[192:193]
	v_pk_mul_f32 v[160:161], v[160:161], v[144:145] op_sel_hi:[1,0]
	v_rcp_f32_e32 v174, v174
	v_pk_mul_f32 v[162:163], v[162:163], v[144:145] op_sel_hi:[1,0]
	v_pk_add_f32 v[182:183], v[182:183], v[142:143] op_sel:[0,1] op_sel_hi:[1,1]
	v_pk_add_f32 v[198:199], v[198:199], v[142:143] op_sel:[0,1] op_sel_hi:[1,1]
	v_pk_mul_f32 v[184:185], v[172:173], v[142:143] op_sel_hi:[1,0]
	v_pk_mul_f32 v[186:187], v[16:17], v[250:251] op_sel:[0,1] op_sel_hi:[1,1]
	v_pk_mul_f32 v[188:189], v[6:7], v[250:251] op_sel:[0,1] op_sel_hi:[1,1]
	v_med3_f32 v157, v157, s87, v227
	v_med3_f32 v160, v160, s87, v227
	v_med3_f32 v162, v162, s87, v227
	v_pk_mul_f32 v[176:177], v[176:177], v[194:195]
	v_rcp_f32_e32 v182, v182
	v_pk_add_f32 v[202:203], v[202:203], v[142:143] op_sel:[0,1] op_sel_hi:[1,1]
	v_pk_mul_f32 v[176:177], v[176:177], v[196:197]
	v_rcp_f32_e32 v198, v198
	v_pk_mul_f32 v[190:191], v[186:187], v[142:143] op_sel_hi:[1,0]
	v_pk_mul_f32 v[176:177], v[176:177], v[144:145] op_sel_hi:[1,0]
	v_exp_f32_e32 v184, v184
	v_pk_mul_f32 v[192:193], v[188:189], v[142:143] op_sel_hi:[1,0]
	v_pk_mul_f32 v[194:195], v[8:9], v[250:251] op_sel:[0,1] op_sel_hi:[1,1]
	v_cvt_pk_fp8_f32 v156, v156, v157
	v_med3_f32 v161, v161, s87, v227
	v_med3_f32 v163, v163, s87, v227
	v_med3_f32 v176, v176, s87, v227
	v_rcp_f32_e32 v202, v202
	v_pk_mul_f32 v[196:197], v[194:195], v[142:143] op_sel_hi:[1,0]
	v_exp_f32_e32 v190, v190
	v_cvt_pk_fp8_f32 v156, v160, v161 op_sel:[0,0,1]
	v_exp_f32_e32 v192, v192
	v_cvt_pk_fp8_f32 v157, v162, v163
	v_rcp_f32_e32 v175, v175
	v_med3_f32 v177, v177, s87, v227
	v_exp_f32_e32 v196, v196
	v_add_u32_e32 v160, 0x70000, v219
	v_rcp_f32_e32 v183, v183
	v_cvt_pk_fp8_f32 v157, v176, v177 op_sel:[0,0,1]
	global_store_dwordx2 v160, v[158:159], s[26:27]
	v_rcp_f32_e32 v199, v199
	v_pk_mul_f32 v[158:159], v[26:27], v[250:251] op_sel_hi:[1,0]
	v_exp_f32_e32 v185, v185
	v_pk_mul_f32 v[160:161], v[28:29], v[250:251] op_sel_hi:[1,0]
	v_rcp_f32_e32 v203, v203
	v_pk_mul_f32 v[158:159], v[158:159], v[170:171]
	v_exp_f32_e32 v191, v191
	v_pk_mul_f32 v[162:163], v[18:19], v[250:251] op_sel_hi:[1,0]
	v_exp_f32_e32 v193, v193
	v_pk_mul_f32 v[158:159], v[158:159], v[174:175]
	v_exp_f32_e32 v197, v197
	v_pk_add_f32 v[184:185], v[184:185], v[142:143] op_sel:[0,1] op_sel_hi:[1,1]
	v_pk_mul_f32 v[158:159], v[158:159], v[144:145] op_sel_hi:[1,0]
	v_pk_mul_f32 v[160:161], v[160:161], v[178:179]
	v_pk_mul_f32 v[162:163], v[162:163], v[180:181]
	v_med3_f32 v158, v158, s87, v227
	v_pk_mul_f32 v[160:161], v[160:161], v[182:183]
	v_pk_mul_f32 v[162:163], v[162:163], v[198:199]
	v_pk_mul_f32 v[170:171], v[20:21], v[250:251] op_sel_hi:[1,0]
	v_pk_mul_f32 v[160:161], v[160:161], v[144:145] op_sel_hi:[1,0]
	v_pk_mul_f32 v[162:163], v[162:163], v[144:145] op_sel_hi:[1,0]
	v_rcp_f32_e32 v184, v184
	v_pk_add_f32 v[190:191], v[190:191], v[142:143] op_sel:[0,1] op_sel_hi:[1,1]
	v_pk_add_f32 v[192:193], v[192:193], v[142:143] op_sel:[0,1] op_sel_hi:[1,1]
	v_med3_f32 v159, v159, s87, v227
	v_med3_f32 v160, v160, s87, v227
	v_med3_f32 v162, v162, s87, v227
	v_pk_mul_f32 v[170:171], v[170:171], v[200:201]
	v_rcp_f32_e32 v190, v190
	v_pk_add_f32 v[196:197], v[196:197], v[142:143] op_sel:[0,1] op_sel_hi:[1,1]
	v_pk_mul_f32 v[170:171], v[170:171], v[202:203]
	v_rcp_f32_e32 v192, v192
	v_cvt_pk_fp8_f32 v158, v158, v159
	v_pk_mul_f32 v[170:171], v[170:171], v[144:145] op_sel_hi:[1,0]
	v_med3_f32 v161, v161, s87, v227
	v_med3_f32 v163, v163, s87, v227
	v_med3_f32 v170, v170, s87, v227
	v_rcp_f32_e32 v196, v196
	v_cvt_pk_fp8_f32 v158, v160, v161 op_sel:[0,0,1]
	v_rcp_f32_e32 v185, v185
	v_cvt_pk_fp8_f32 v159, v162, v163
	v_med3_f32 v171, v171, s87, v227
	v_add_u32_e32 v160, 0x7e000, v219
	v_rcp_f32_e32 v191, v191
	v_cvt_pk_fp8_f32 v159, v170, v171 op_sel:[0,0,1]
	global_store_dwordx2 v160, v[156:157], s[26:27]
	v_rcp_f32_e32 v193, v193
	v_pk_mul_f32 v[156:157], v[10:11], v[250:251] op_sel:[0,1] op_sel_hi:[1,1]
	v_rcp_f32_e32 v197, v197
	v_pk_mul_f32 v[160:161], v[12:13], v[250:251] op_sel:[0,1] op_sel_hi:[1,1]
	v_pk_mul_f32 v[156:157], v[156:157], v[172:173]
	v_pk_mul_f32 v[162:163], v[2:3], v[250:251] op_sel:[0,1] op_sel_hi:[1,1]
	v_pk_mul_f32 v[160:161], v[160:161], v[186:187]
	v_pk_mul_f32 v[156:157], v[156:157], v[184:185]
	v_pk_mul_f32 v[162:163], v[162:163], v[188:189]
	v_pk_mul_f32 v[160:161], v[160:161], v[190:191]
	v_pk_mul_f32 v[156:157], v[156:157], v[144:145] op_sel_hi:[1,0]
	v_pk_mul_f32 v[162:163], v[162:163], v[192:193]
	v_pk_mul_f32 v[160:161], v[160:161], v[144:145] op_sel_hi:[1,0]
	v_med3_f32 v156, v156, s87, v227
	v_pk_mul_f32 v[162:163], v[162:163], v[144:145] op_sel_hi:[1,0]
	v_pk_mul_f32 v[170:171], v[4:5], v[250:251] op_sel:[0,1] op_sel_hi:[1,1]
	v_med3_f32 v157, v157, s87, v227
	v_med3_f32 v160, v160, s87, v227
	v_med3_f32 v162, v162, s87, v227
	v_pk_mul_f32 v[170:171], v[170:171], v[194:195]
	v_cvt_pk_fp8_f32 v156, v156, v157
	v_med3_f32 v161, v161, s87, v227
	v_pk_mul_f32 v[170:171], v[170:171], v[196:197]
	v_med3_f32 v163, v163, s87, v227
	v_cvt_pk_fp8_f32 v156, v160, v161 op_sel:[0,0,1]
	v_pk_mul_f32 v[170:171], v[170:171], v[144:145] op_sel_hi:[1,0]
	v_cvt_pk_fp8_f32 v157, v162, v163
	v_add_u32_e32 v160, 0x8c000, v219
	v_med3_f32 v170, v170, s87, v227
	v_add_u32_e32 v161, 0x9a000, v219
	global_store_dwordx2 v160, v[158:159], s[26:27]
	v_med3_f32 v171, v171, s87, v227
	v_cvt_pk_fp8_f32 v157, v170, v171 op_sel:[0,0,1]
	global_store_dwordx2 v161, v[156:157], s[26:27]
	s_andn2_b64 vcc, exec, s[46:47]
	s_mov_b64 s[46:47], -1
	s_cbranch_vccnz .LBB0_807
	s_andn2_b64 vcc, exec, s[30:31]
	s_cbranch_vccnz .LBB0_806
	s_barrier
	s_branch .LBB0_806

.LBB0_845:
	v_xor_b32_e32 v240, 16, v231
	v_and_b32_e32 v238, 64, v231
	v_add_u32_e32 v238, 64, v238
	v_xor_b32_e32 v239, 32, v231
	v_cmp_lt_i32_e32 vcc, v240, v238
	v_mov_b32_e32 v2, 0xbfb8aa3b
	v_mov_b32_e32 v3, 1.0
	v_cndmask_b32_e32 v240, v231, v240, vcc
	v_cmp_lt_i32_e32 vcc, v239, v238
	v_lshlrev_b32_e32 v240, 2, v240
	v_mov_b32_e32 v4, 0x41000000
	v_cndmask_b32_e32 v239, v231, v239, vcc
	v_lshlrev_b32_e32 v239, 2, v239
	ds_bpermute_b32 v6, v240, v244
	ds_bpermute_b32 v7, v240, v245
	ds_bpermute_b32 v8, v240, v246
	ds_bpermute_b32 v9, v240, v247
	ds_bpermute_b32 v10, v240, v248
	ds_bpermute_b32 v11, v240, v249
	ds_bpermute_b32 v12, v240, v250
	ds_bpermute_b32 v13, v240, v251
	v_lshl_add_u32 v243, s50, 8, v195
	v_lshl_or_b32 v242, s61, 7, v197
	v_mad_u32_u24 v241, v243, s33, v242
	s_waitcnt lgkmcnt(7)
	v_add_f32_e32 v244, v244, v6
	ds_bpermute_b32 v6, v239, v244
	s_waitcnt lgkmcnt(7)
	v_add_f32_e32 v245, v245, v7
	ds_bpermute_b32 v7, v239, v245
	s_waitcnt lgkmcnt(7)
	v_add_f32_e32 v246, v246, v8
	ds_bpermute_b32 v8, v239, v246
	s_waitcnt lgkmcnt(7)
	v_add_f32_e32 v247, v247, v9
	ds_bpermute_b32 v9, v239, v247
	s_waitcnt lgkmcnt(7)
	v_add_f32_e32 v248, v248, v10
	ds_bpermute_b32 v10, v239, v248
	s_waitcnt lgkmcnt(7)
	v_add_f32_e32 v249, v249, v11
	ds_bpermute_b32 v11, v239, v249
	s_waitcnt lgkmcnt(7)
	v_add_f32_e32 v250, v250, v12
	ds_bpermute_b32 v12, v239, v250
	s_waitcnt lgkmcnt(7)
	v_add_f32_e32 v251, v251, v13
	ds_bpermute_b32 v13, v239, v251
	s_waitcnt lgkmcnt(7)
	v_add_f32_e32 v244, v244, v6
	v_fmamk_f32 v244, v244, 0x3a800000, v224
	s_waitcnt lgkmcnt(6)
	v_add_f32_e32 v245, v245, v7
	v_fmamk_f32 v245, v245, 0x3a800000, v224
	s_waitcnt lgkmcnt(5)
	v_add_f32_e32 v246, v246, v8
	v_fmamk_f32 v246, v246, 0x3a800000, v224
	s_waitcnt lgkmcnt(4)
	v_add_f32_e32 v247, v247, v9
	v_fmamk_f32 v247, v247, 0x3a800000, v224
	s_waitcnt lgkmcnt(3)
	v_add_f32_e32 v248, v248, v10
	v_fmamk_f32 v248, v248, 0x3a800000, v224
	s_waitcnt lgkmcnt(2)
	v_add_f32_e32 v249, v249, v11
	v_fmamk_f32 v249, v249, 0x3a800000, v224
	s_waitcnt lgkmcnt(1)
	v_add_f32_e32 v250, v250, v12
	v_fmamk_f32 v250, v250, 0x3a800000, v224
	s_waitcnt lgkmcnt(0)
	v_add_f32_e32 v251, v251, v13
	v_fmamk_f32 v251, v251, 0x3a800000, v224
	v_rsq_f32_e32 v244, v244
	v_rsq_f32_e32 v245, v245
	v_rsq_f32_e32 v246, v246
	v_rsq_f32_e32 v247, v247
	v_rsq_f32_e32 v248, v248
	v_rsq_f32_e32 v249, v249
	v_rsq_f32_e32 v250, v250
	v_rsq_f32_e32 v251, v251
	v_pk_mul_f32 v[6:7], v[158:159], v[244:245] op_sel_hi:[1,0]
	v_pk_mul_f32 v[8:9], v[160:161], v[244:245] op_sel_hi:[1,0]
	v_pk_mul_f32 v[10:11], v[150:151], v[244:245] op_sel_hi:[1,0]
	v_pk_mul_f32 v[12:13], v[6:7], v[2:3] op_sel_hi:[1,0]
	v_pk_mul_f32 v[14:15], v[8:9], v[2:3] op_sel_hi:[1,0]
	v_pk_mul_f32 v[16:17], v[10:11], v[2:3] op_sel_hi:[1,0]
	v_exp_f32_e32 v12, v12
	v_pk_mul_f32 v[18:19], v[152:153], v[244:245] op_sel_hi:[1,0]
	v_exp_f32_e32 v14, v14
	v_pk_mul_f32 v[20:21], v[142:143], v[244:245] op_sel:[0,1] op_sel_hi:[1,1]
	v_exp_f32_e32 v16, v16
	v_pk_mul_f32 v[22:23], v[18:19], v[2:3] op_sel_hi:[1,0]
	v_pk_mul_f32 v[24:25], v[20:21], v[2:3] op_sel_hi:[1,0]
	v_pk_mul_f32 v[26:27], v[144:145], v[244:245] op_sel:[0,1] op_sel_hi:[1,1]
	v_exp_f32_e32 v22, v22
	v_pk_mul_f32 v[28:29], v[134:135], v[244:245] op_sel:[0,1] op_sel_hi:[1,1]
	v_exp_f32_e32 v13, v13
	v_pk_mul_f32 v[30:31], v[26:27], v[2:3] op_sel_hi:[1,0]
	v_exp_f32_e32 v15, v15
	v_pk_mul_f32 v[32:33], v[28:29], v[2:3] op_sel_hi:[1,0]
	v_exp_f32_e32 v17, v17
	v_pk_mul_f32 v[186:187], v[136:137], v[244:245] op_sel:[0,1] op_sel_hi:[1,1]
	v_exp_f32_e32 v23, v23
	v_pk_mul_f32 v[188:189], v[154:155], v[244:245] op_sel_hi:[1,0]
	v_pk_add_f32 v[12:13], v[12:13], v[2:3] op_sel:[0,1] op_sel_hi:[1,1]
	v_exp_f32_e32 v24, v24
	v_pk_add_f32 v[14:15], v[14:15], v[2:3] op_sel:[0,1] op_sel_hi:[1,1]
	v_rcp_f32_e32 v12, v12
	v_pk_add_f32 v[16:17], v[16:17], v[2:3] op_sel:[0,1] op_sel_hi:[1,1]
	v_rcp_f32_e32 v14, v14
	v_pk_add_f32 v[22:23], v[22:23], v[2:3] op_sel:[0,1] op_sel_hi:[1,1]
	v_rcp_f32_e32 v16, v16
	v_pk_mul_f32 v[190:191], v[186:187], v[2:3] op_sel_hi:[1,0]
	v_rcp_f32_e32 v22, v22
	v_pk_mul_f32 v[188:189], v[188:189], v[6:7]
	v_exp_f32_e32 v30, v30
	v_pk_mul_f32 v[6:7], v[156:157], v[244:245] op_sel_hi:[1,0]
	v_exp_f32_e32 v32, v32
	v_pk_mul_f32 v[192:193], v[146:147], v[244:245] op_sel_hi:[1,0]
	v_rcp_f32_e32 v13, v13
	v_pk_mul_f32 v[200:201], v[126:127], v[246:247] op_sel_hi:[1,0]
	v_exp_f32_e32 v190, v190
	v_pk_mul_f32 v[6:7], v[6:7], v[8:9]
	v_rcp_f32_e32 v15, v15
	v_pk_mul_f32 v[192:193], v[192:193], v[10:11]
	v_rcp_f32_e32 v17, v17
	v_pk_mul_f32 v[8:9], v[148:149], v[244:245] op_sel_hi:[1,0]
	v_exp_f32_e32 v25, v25
	v_pk_mul_f32 v[188:189], v[188:189], v[12:13]
	v_rcp_f32_e32 v23, v23
	v_pk_mul_f32 v[10:11], v[200:201], v[2:3] op_sel_hi:[1,0]
	v_exp_f32_e32 v31, v31
	v_pk_mul_f32 v[188:189], v[188:189], v[4:5] op_sel_hi:[1,0]
	v_exp_f32_e32 v33, v33
	v_pk_mul_f32 v[6:7], v[6:7], v[14:15]
	v_exp_f32_e32 v191, v191
	v_pk_mul_f32 v[192:193], v[192:193], v[16:17]
	v_pk_add_f32 v[24:25], v[24:25], v[2:3] op_sel:[0,1] op_sel_hi:[1,1]
	v_med3_f32 v188, v188, s87, v227
	v_pk_mul_f32 v[6:7], v[6:7], v[4:5] op_sel_hi:[1,0]
	v_pk_mul_f32 v[192:193], v[192:193], v[4:5] op_sel_hi:[1,0]
	v_rcp_f32_e32 v24, v24
	v_pk_add_f32 v[30:31], v[30:31], v[2:3] op_sel:[0,1] op_sel_hi:[1,1]
	v_pk_add_f32 v[32:33], v[32:33], v[2:3] op_sel:[0,1] op_sel_hi:[1,1]
	v_pk_mul_f32 v[12:13], v[128:129], v[246:247] op_sel_hi:[1,0]
	v_pk_mul_f32 v[14:15], v[118:119], v[246:247] op_sel_hi:[1,0]
	v_med3_f32 v189, v189, s87, v227
	v_med3_f32 v6, v6, s87, v227
	v_med3_f32 v192, v192, s87, v227
	v_pk_mul_f32 v[8:9], v[8:9], v[18:19]
	v_rcp_f32_e32 v30, v30
	v_pk_add_f32 v[190:191], v[190:191], v[2:3] op_sel:[0,1] op_sel_hi:[1,1]
	v_pk_mul_f32 v[8:9], v[8:9], v[22:23]
	v_rcp_f32_e32 v32, v32
	v_pk_mul_f32 v[16:17], v[12:13], v[2:3] op_sel_hi:[1,0]
	v_pk_mul_f32 v[8:9], v[8:9], v[4:5] op_sel_hi:[1,0]
	v_exp_f32_e32 v10, v10
	v_pk_mul_f32 v[18:19], v[14:15], v[2:3] op_sel_hi:[1,0]
	v_pk_mul_f32 v[22:23], v[120:121], v[246:247] op_sel_hi:[1,0]
	v_cvt_pk_fp8_f32 v188, v188, v189
	v_med3_f32 v7, v7, s87, v227
	v_med3_f32 v193, v193, s87, v227
	v_med3_f32 v8, v8, s87, v227
	v_rcp_f32_e32 v190, v190
	v_pk_mul_f32 v[202:203], v[22:23], v[2:3] op_sel_hi:[1,0]
	v_exp_f32_e32 v16, v16
	v_cvt_pk_fp8_f32 v188, v6, v7 op_sel:[0,0,1]
	v_exp_f32_e32 v18, v18
	v_cvt_pk_fp8_f32 v189, v192, v193
	v_rcp_f32_e32 v25, v25
	v_med3_f32 v9, v9, s87, v227
	v_exp_f32_e32 v202, v202
	v_pk_mul_f32 v[6:7], v[138:139], v[244:245] op_sel:[0,1] op_sel_hi:[1,1]
	v_rcp_f32_e32 v31, v31
	v_cvt_pk_fp8_f32 v189, v8, v9 op_sel:[0,0,1]
	v_rcp_f32_e32 v33, v33
	v_pk_mul_f32 v[6:7], v[6:7], v[20:21]
	v_exp_f32_e32 v11, v11
	global_store_dwordx2 v241, v[188:189], s[26:27]
	v_rcp_f32_e32 v191, v191
	v_pk_mul_f32 v[6:7], v[6:7], v[24:25]
	v_exp_f32_e32 v17, v17
	v_pk_mul_f32 v[8:9], v[140:141], v[244:245] op_sel:[0,1] op_sel_hi:[1,1]
	v_exp_f32_e32 v19, v19
	v_pk_mul_f32 v[6:7], v[6:7], v[4:5] op_sel_hi:[1,0]
	v_exp_f32_e32 v203, v203
	v_pk_mul_f32 v[20:21], v[130:131], v[244:245] op_sel:[0,1] op_sel_hi:[1,1]
	v_pk_add_f32 v[10:11], v[10:11], v[2:3] op_sel:[0,1] op_sel_hi:[1,1]
	v_pk_mul_f32 v[24:25], v[110:111], v[246:247] op_sel:[0,1] op_sel_hi:[1,1]
	v_med3_f32 v6, v6, s87, v227
	v_pk_mul_f32 v[8:9], v[8:9], v[26:27]
	v_pk_mul_f32 v[20:21], v[20:21], v[28:29]
	v_pk_mul_f32 v[26:27], v[132:133], v[244:245] op_sel:[0,1] op_sel_hi:[1,1]
	v_pk_mul_f32 v[8:9], v[8:9], v[30:31]
	v_pk_mul_f32 v[20:21], v[20:21], v[32:33]
	v_rcp_f32_e32 v10, v10
	v_pk_mul_f32 v[8:9], v[8:9], v[4:5] op_sel_hi:[1,0]
	v_pk_mul_f32 v[20:21], v[20:21], v[4:5] op_sel_hi:[1,0]
	v_pk_add_f32 v[16:17], v[16:17], v[2:3] op_sel:[0,1] op_sel_hi:[1,1]
	v_pk_add_f32 v[18:19], v[18:19], v[2:3] op_sel:[0,1] op_sel_hi:[1,1]
	v_pk_mul_f32 v[28:29], v[24:25], v[2:3] op_sel_hi:[1,0]
	v_pk_mul_f32 v[30:31], v[112:113], v[246:247] op_sel:[0,1] op_sel_hi:[1,1]
	v_pk_mul_f32 v[32:33], v[102:103], v[246:247] op_sel:[0,1] op_sel_hi:[1,1]
	v_med3_f32 v7, v7, s87, v227
	v_med3_f32 v8, v8, s87, v227
	v_med3_f32 v20, v20, s87, v227
	v_pk_mul_f32 v[26:27], v[26:27], v[186:187]
	v_rcp_f32_e32 v16, v16
	v_pk_add_f32 v[202:203], v[202:203], v[2:3] op_sel:[0,1] op_sel_hi:[1,1]
	v_pk_mul_f32 v[26:27], v[26:27], v[190:191]
	v_rcp_f32_e32 v18, v18
	v_pk_mul_f32 v[186:187], v[30:31], v[2:3] op_sel_hi:[1,0]
	v_pk_mul_f32 v[26:27], v[26:27], v[4:5] op_sel_hi:[1,0]
	v_exp_f32_e32 v28, v28
	v_pk_mul_f32 v[188:189], v[32:33], v[2:3] op_sel_hi:[1,0]
	v_pk_mul_f32 v[190:191], v[104:105], v[246:247] op_sel:[0,1] op_sel_hi:[1,1]
	v_cvt_pk_fp8_f32 v6, v6, v7
	v_med3_f32 v9, v9, s87, v227
	v_med3_f32 v21, v21, s87, v227
	v_med3_f32 v26, v26, s87, v227
	v_rcp_f32_e32 v202, v202
	v_pk_mul_f32 v[192:193], v[190:191], v[2:3] op_sel_hi:[1,0]
	v_exp_f32_e32 v186, v186
	v_cvt_pk_fp8_f32 v6, v8, v9 op_sel:[0,0,1]
	v_exp_f32_e32 v188, v188
	v_cvt_pk_fp8_f32 v7, v20, v21
	v_rcp_f32_e32 v11, v11
	v_med3_f32 v27, v27, s87, v227
	v_exp_f32_e32 v192, v192
	v_pk_mul_f32 v[8:9], v[122:123], v[246:247] op_sel_hi:[1,0]
	v_rcp_f32_e32 v17, v17
	v_cvt_pk_fp8_f32 v7, v26, v27 op_sel:[0,0,1]
	v_rcp_f32_e32 v19, v19
	v_pk_mul_f32 v[8:9], v[8:9], v[200:201]
	v_exp_f32_e32 v29, v29
	v_pk_mul_f32 v[20:21], v[124:125], v[246:247] op_sel_hi:[1,0]
	v_rcp_f32_e32 v203, v203
	v_pk_mul_f32 v[8:9], v[8:9], v[10:11]
	v_exp_f32_e32 v187, v187
	v_pk_mul_f32 v[10:11], v[114:115], v[246:247] op_sel_hi:[1,0]
	v_exp_f32_e32 v189, v189
	v_pk_mul_f32 v[8:9], v[8:9], v[4:5] op_sel_hi:[1,0]
	v_exp_f32_e32 v193, v193
	v_pk_add_f32 v[28:29], v[28:29], v[2:3] op_sel:[0,1] op_sel_hi:[1,1]
	v_pk_mul_f32 v[26:27], v[94:95], v[248:249] op_sel_hi:[1,0]
	v_med3_f32 v8, v8, s87, v227
	v_pk_mul_f32 v[20:21], v[20:21], v[12:13]
	v_pk_mul_f32 v[10:11], v[10:11], v[14:15]
	v_pk_mul_f32 v[12:13], v[116:117], v[246:247] op_sel_hi:[1,0]
	v_pk_mul_f32 v[20:21], v[20:21], v[16:17]
	v_pk_mul_f32 v[10:11], v[10:11], v[18:19]
	v_rcp_f32_e32 v28, v28
	v_pk_mul_f32 v[20:21], v[20:21], v[4:5] op_sel_hi:[1,0]
	v_pk_mul_f32 v[10:11], v[10:11], v[4:5] op_sel_hi:[1,0]
	v_pk_add_f32 v[186:187], v[186:187], v[2:3] op_sel:[0,1] op_sel_hi:[1,1]
	v_pk_add_f32 v[188:189], v[188:189], v[2:3] op_sel:[0,1] op_sel_hi:[1,1]
	v_pk_mul_f32 v[14:15], v[26:27], v[2:3] op_sel_hi:[1,0]
	v_pk_mul_f32 v[16:17], v[96:97], v[248:249] op_sel_hi:[1,0]
	v_pk_mul_f32 v[18:19], v[86:87], v[248:249] op_sel_hi:[1,0]
	v_med3_f32 v9, v9, s87, v227
	v_med3_f32 v20, v20, s87, v227
	v_med3_f32 v10, v10, s87, v227
	v_pk_mul_f32 v[12:13], v[12:13], v[22:23]
	v_rcp_f32_e32 v186, v186
	v_pk_add_f32 v[192:193], v[192:193], v[2:3] op_sel:[0,1] op_sel_hi:[1,1]
	v_pk_mul_f32 v[12:13], v[12:13], v[202:203]
	v_rcp_f32_e32 v188, v188
	v_pk_mul_f32 v[22:23], v[16:17], v[2:3] op_sel_hi:[1,0]
	v_pk_mul_f32 v[12:13], v[12:13], v[4:5] op_sel_hi:[1,0]
	v_exp_f32_e32 v14, v14
	v_pk_mul_f32 v[200:201], v[18:19], v[2:3] op_sel_hi:[1,0]
	v_pk_mul_f32 v[202:203], v[88:89], v[248:249] op_sel_hi:[1,0]
	v_cvt_pk_fp8_f32 v8, v8, v9
	v_med3_f32 v21, v21, s87, v227
	v_med3_f32 v11, v11, s87, v227
	v_med3_f32 v12, v12, s87, v227
	v_rcp_f32_e32 v192, v192
	v_pk_mul_f32 v[204:205], v[202:203], v[2:3] op_sel_hi:[1,0]
	v_exp_f32_e32 v22, v22
	v_cvt_pk_fp8_f32 v8, v20, v21 op_sel:[0,0,1]
	v_exp_f32_e32 v200, v200
	v_cvt_pk_fp8_f32 v9, v10, v11
	v_rcp_f32_e32 v29, v29
	v_med3_f32 v13, v13, s87, v227
	v_exp_f32_e32 v204, v204
	v_add_u32_e32 v10, 0xe000, v241
	v_rcp_f32_e32 v187, v187
	v_cvt_pk_fp8_f32 v9, v12, v13 op_sel:[0,0,1]
	global_store_dwordx2 v10, v[6:7], s[26:27]
	v_rcp_f32_e32 v189, v189
	v_pk_mul_f32 v[6:7], v[106:107], v[246:247] op_sel:[0,1] op_sel_hi:[1,1]
	v_exp_f32_e32 v15, v15
	v_pk_mul_f32 v[10:11], v[108:109], v[246:247] op_sel:[0,1] op_sel_hi:[1,1]
	v_rcp_f32_e32 v193, v193
	v_pk_mul_f32 v[6:7], v[6:7], v[24:25]
	v_exp_f32_e32 v23, v23
	v_pk_mul_f32 v[12:13], v[98:99], v[246:247] op_sel:[0,1] op_sel_hi:[1,1]
	v_exp_f32_e32 v201, v201
	v_pk_mul_f32 v[6:7], v[6:7], v[28:29]
	v_exp_f32_e32 v205, v205
	v_pk_add_f32 v[14:15], v[14:15], v[2:3] op_sel:[0,1] op_sel_hi:[1,1]
	v_pk_mul_f32 v[6:7], v[6:7], v[4:5] op_sel_hi:[1,0]
	v_pk_mul_f32 v[20:21], v[78:79], v[248:249] op_sel:[0,1] op_sel_hi:[1,1]
	v_pk_mul_f32 v[10:11], v[10:11], v[30:31]
	v_med3_f32 v6, v6, s87, v227
	v_pk_mul_f32 v[12:13], v[12:13], v[32:33]
	v_pk_mul_f32 v[10:11], v[10:11], v[186:187]
	v_pk_mul_f32 v[24:25], v[100:101], v[246:247] op_sel:[0,1] op_sel_hi:[1,1]
	v_pk_mul_f32 v[12:13], v[12:13], v[188:189]
	v_pk_mul_f32 v[10:11], v[10:11], v[4:5] op_sel_hi:[1,0]
	v_rcp_f32_e32 v14, v14
	v_pk_mul_f32 v[12:13], v[12:13], v[4:5] op_sel_hi:[1,0]
	v_pk_add_f32 v[22:23], v[22:23], v[2:3] op_sel:[0,1] op_sel_hi:[1,1]
	v_pk_add_f32 v[200:201], v[200:201], v[2:3] op_sel:[0,1] op_sel_hi:[1,1]
	v_pk_mul_f32 v[28:29], v[20:21], v[2:3] op_sel_hi:[1,0]
	v_pk_mul_f32 v[30:31], v[80:81], v[248:249] op_sel:[0,1] op_sel_hi:[1,1]
	v_pk_mul_f32 v[32:33], v[70:71], v[248:249] op_sel:[0,1] op_sel_hi:[1,1]
	v_med3_f32 v7, v7, s87, v227
	v_med3_f32 v10, v10, s87, v227
	v_med3_f32 v12, v12, s87, v227
	v_pk_mul_f32 v[24:25], v[24:25], v[190:191]
	v_rcp_f32_e32 v22, v22
	v_pk_add_f32 v[204:205], v[204:205], v[2:3] op_sel:[0,1] op_sel_hi:[1,1]
	v_pk_mul_f32 v[24:25], v[24:25], v[192:193]
	v_rcp_f32_e32 v200, v200
	v_pk_mul_f32 v[186:187], v[30:31], v[2:3] op_sel_hi:[1,0]
	v_pk_mul_f32 v[24:25], v[24:25], v[4:5] op_sel_hi:[1,0]
	v_exp_f32_e32 v28, v28
	v_pk_mul_f32 v[188:189], v[32:33], v[2:3] op_sel_hi:[1,0]
	v_pk_mul_f32 v[190:191], v[72:73], v[248:249] op_sel:[0,1] op_sel_hi:[1,1]
	v_cvt_pk_fp8_f32 v6, v6, v7
	v_med3_f32 v11, v11, s87, v227
	v_med3_f32 v13, v13, s87, v227
	v_med3_f32 v24, v24, s87, v227
	v_rcp_f32_e32 v204, v204
	v_pk_mul_f32 v[192:193], v[190:191], v[2:3] op_sel_hi:[1,0]
	v_exp_f32_e32 v186, v186
	v_cvt_pk_fp8_f32 v6, v10, v11 op_sel:[0,0,1]
	v_exp_f32_e32 v188, v188
	v_cvt_pk_fp8_f32 v7, v12, v13
	v_rcp_f32_e32 v15, v15
	v_med3_f32 v25, v25, s87, v227
	v_exp_f32_e32 v192, v192
	v_add_u32_e32 v10, 0x1c000, v241
	v_rcp_f32_e32 v23, v23
	v_cvt_pk_fp8_f32 v7, v24, v25 op_sel:[0,0,1]
	global_store_dwordx2 v10, v[8:9], s[26:27]
	v_rcp_f32_e32 v201, v201
	v_pk_mul_f32 v[8:9], v[90:91], v[248:249] op_sel_hi:[1,0]
	v_exp_f32_e32 v29, v29
	v_pk_mul_f32 v[10:11], v[92:93], v[248:249] op_sel_hi:[1,0]
	v_rcp_f32_e32 v205, v205
	v_pk_mul_f32 v[8:9], v[8:9], v[26:27]
	v_exp_f32_e32 v187, v187
	v_pk_mul_f32 v[12:13], v[82:83], v[248:249] op_sel_hi:[1,0]
	v_exp_f32_e32 v189, v189
	v_pk_mul_f32 v[8:9], v[8:9], v[14:15]
	v_exp_f32_e32 v193, v193
	v_pk_add_f32 v[28:29], v[28:29], v[2:3] op_sel:[0,1] op_sel_hi:[1,1]
	v_pk_mul_f32 v[8:9], v[8:9], v[4:5] op_sel_hi:[1,0]
	v_pk_mul_f32 v[14:15], v[62:63], v[250:251] op_sel_hi:[1,0]
	v_pk_mul_f32 v[10:11], v[10:11], v[16:17]
	v_med3_f32 v8, v8, s87, v227
	v_pk_mul_f32 v[12:13], v[12:13], v[18:19]
	v_pk_mul_f32 v[10:11], v[10:11], v[22:23]
	v_pk_mul_f32 v[16:17], v[84:85], v[248:249] op_sel_hi:[1,0]
	v_pk_mul_f32 v[12:13], v[12:13], v[200:201]
	v_pk_mul_f32 v[10:11], v[10:11], v[4:5] op_sel_hi:[1,0]
	v_rcp_f32_e32 v28, v28
	v_pk_mul_f32 v[12:13], v[12:13], v[4:5] op_sel_hi:[1,0]
	v_pk_add_f32 v[186:187], v[186:187], v[2:3] op_sel:[0,1] op_sel_hi:[1,1]
	v_pk_add_f32 v[188:189], v[188:189], v[2:3] op_sel:[0,1] op_sel_hi:[1,1]
	v_pk_mul_f32 v[18:19], v[14:15], v[2:3] op_sel_hi:[1,0]
	v_pk_mul_f32 v[22:23], v[64:65], v[250:251] op_sel_hi:[1,0]
	v_pk_mul_f32 v[24:25], v[54:55], v[250:251] op_sel_hi:[1,0]
	v_med3_f32 v9, v9, s87, v227
	v_med3_f32 v10, v10, s87, v227
	v_med3_f32 v12, v12, s87, v227
	v_pk_mul_f32 v[16:17], v[16:17], v[202:203]
	v_rcp_f32_e32 v186, v186
	v_pk_add_f32 v[192:193], v[192:193], v[2:3] op_sel:[0,1] op_sel_hi:[1,1]
	v_pk_mul_f32 v[16:17], v[16:17], v[204:205]
	v_rcp_f32_e32 v188, v188
	v_pk_mul_f32 v[26:27], v[22:23], v[2:3] op_sel_hi:[1,0]
	v_pk_mul_f32 v[16:17], v[16:17], v[4:5] op_sel_hi:[1,0]
	v_exp_f32_e32 v18, v18
	v_pk_mul_f32 v[200:201], v[24:25], v[2:3] op_sel_hi:[1,0]
	v_pk_mul_f32 v[202:203], v[56:57], v[250:251] op_sel_hi:[1,0]
	v_cvt_pk_fp8_f32 v8, v8, v9
	v_med3_f32 v11, v11, s87, v227
	v_med3_f32 v13, v13, s87, v227
	v_med3_f32 v16, v16, s87, v227
	v_rcp_f32_e32 v192, v192
	v_pk_mul_f32 v[204:205], v[202:203], v[2:3] op_sel_hi:[1,0]
	v_exp_f32_e32 v26, v26
	v_cvt_pk_fp8_f32 v8, v10, v11 op_sel:[0,0,1]
	v_exp_f32_e32 v200, v200
	v_cvt_pk_fp8_f32 v9, v12, v13
	v_rcp_f32_e32 v29, v29
	v_med3_f32 v17, v17, s87, v227
	v_exp_f32_e32 v204, v204
	v_add_u32_e32 v10, 0x2a000, v241
	v_rcp_f32_e32 v187, v187
	v_cvt_pk_fp8_f32 v9, v16, v17 op_sel:[0,0,1]
	global_store_dwordx2 v10, v[6:7], s[26:27]
	v_rcp_f32_e32 v189, v189
	v_pk_mul_f32 v[6:7], v[74:75], v[248:249] op_sel:[0,1] op_sel_hi:[1,1]
	v_exp_f32_e32 v19, v19
	v_pk_mul_f32 v[10:11], v[76:77], v[248:249] op_sel:[0,1] op_sel_hi:[1,1]
	v_rcp_f32_e32 v193, v193
	v_pk_mul_f32 v[6:7], v[6:7], v[20:21]
	v_exp_f32_e32 v27, v27
	v_pk_mul_f32 v[12:13], v[66:67], v[248:249] op_sel:[0,1] op_sel_hi:[1,1]
	v_exp_f32_e32 v201, v201
	v_pk_mul_f32 v[6:7], v[6:7], v[28:29]
	v_exp_f32_e32 v205, v205
	v_pk_add_f32 v[18:19], v[18:19], v[2:3] op_sel:[0,1] op_sel_hi:[1,1]
	v_pk_mul_f32 v[6:7], v[6:7], v[4:5] op_sel_hi:[1,0]
	v_pk_mul_f32 v[16:17], v[46:47], v[250:251] op_sel:[0,1] op_sel_hi:[1,1]
	v_pk_mul_f32 v[10:11], v[10:11], v[30:31]
	v_med3_f32 v6, v6, s87, v227
	v_pk_mul_f32 v[12:13], v[12:13], v[32:33]
	v_pk_mul_f32 v[10:11], v[10:11], v[186:187]
	v_pk_mul_f32 v[20:21], v[68:69], v[248:249] op_sel:[0,1] op_sel_hi:[1,1]
	v_pk_mul_f32 v[12:13], v[12:13], v[188:189]
	v_pk_mul_f32 v[10:11], v[10:11], v[4:5] op_sel_hi:[1,0]
	v_rcp_f32_e32 v18, v18
	v_pk_mul_f32 v[12:13], v[12:13], v[4:5] op_sel_hi:[1,0]
	v_pk_add_f32 v[26:27], v[26:27], v[2:3] op_sel:[0,1] op_sel_hi:[1,1]
	v_pk_add_f32 v[200:201], v[200:201], v[2:3] op_sel:[0,1] op_sel_hi:[1,1]
	v_pk_mul_f32 v[28:29], v[16:17], v[2:3] op_sel_hi:[1,0]
	v_pk_mul_f32 v[30:31], v[48:49], v[250:251] op_sel:[0,1] op_sel_hi:[1,1]
	v_pk_mul_f32 v[32:33], v[38:39], v[250:251] op_sel:[0,1] op_sel_hi:[1,1]
	v_med3_f32 v7, v7, s87, v227
	v_med3_f32 v10, v10, s87, v227
	v_med3_f32 v12, v12, s87, v227
	v_pk_mul_f32 v[20:21], v[20:21], v[190:191]
	v_rcp_f32_e32 v26, v26
	v_pk_add_f32 v[204:205], v[204:205], v[2:3] op_sel:[0,1] op_sel_hi:[1,1]
	v_pk_mul_f32 v[20:21], v[20:21], v[192:193]
	v_rcp_f32_e32 v200, v200
	v_pk_mul_f32 v[186:187], v[30:31], v[2:3] op_sel_hi:[1,0]
	v_pk_mul_f32 v[20:21], v[20:21], v[4:5] op_sel_hi:[1,0]
	v_exp_f32_e32 v28, v28
	v_pk_mul_f32 v[188:189], v[32:33], v[2:3] op_sel_hi:[1,0]
	v_pk_mul_f32 v[190:191], v[40:41], v[250:251] op_sel:[0,1] op_sel_hi:[1,1]
	v_cvt_pk_fp8_f32 v6, v6, v7
	v_med3_f32 v11, v11, s87, v227
	v_med3_f32 v13, v13, s87, v227
	v_med3_f32 v20, v20, s87, v227
	v_rcp_f32_e32 v204, v204
	v_pk_mul_f32 v[192:193], v[190:191], v[2:3] op_sel_hi:[1,0]
	v_exp_f32_e32 v186, v186
	v_cvt_pk_fp8_f32 v6, v10, v11 op_sel:[0,0,1]
	v_exp_f32_e32 v188, v188
	v_cvt_pk_fp8_f32 v7, v12, v13
	v_rcp_f32_e32 v19, v19
	v_med3_f32 v21, v21, s87, v227
	v_exp_f32_e32 v192, v192
	v_add_u32_e32 v10, 0x70000, v241
	v_rcp_f32_e32 v27, v27
	v_cvt_pk_fp8_f32 v7, v20, v21 op_sel:[0,0,1]
	global_store_dwordx2 v10, v[8:9], s[26:27]
	v_rcp_f32_e32 v201, v201
	v_pk_mul_f32 v[8:9], v[58:59], v[250:251] op_sel_hi:[1,0]
	v_exp_f32_e32 v29, v29
	v_pk_mul_f32 v[10:11], v[60:61], v[250:251] op_sel_hi:[1,0]
	v_rcp_f32_e32 v205, v205
	v_pk_mul_f32 v[8:9], v[8:9], v[14:15]
	v_exp_f32_e32 v187, v187
	v_pk_mul_f32 v[12:13], v[50:51], v[250:251] op_sel_hi:[1,0]
	v_exp_f32_e32 v189, v189
	v_pk_mul_f32 v[8:9], v[8:9], v[18:19]
	v_exp_f32_e32 v193, v193
	v_pk_add_f32 v[28:29], v[28:29], v[2:3] op_sel:[0,1] op_sel_hi:[1,1]
	v_pk_mul_f32 v[8:9], v[8:9], v[4:5] op_sel_hi:[1,0]
	v_pk_mul_f32 v[10:11], v[10:11], v[22:23]
	v_pk_mul_f32 v[12:13], v[12:13], v[24:25]
	v_med3_f32 v8, v8, s87, v227
	v_pk_mul_f32 v[10:11], v[10:11], v[26:27]
	v_pk_mul_f32 v[12:13], v[12:13], v[200:201]
	v_pk_mul_f32 v[14:15], v[52:53], v[250:251] op_sel_hi:[1,0]
	v_pk_mul_f32 v[10:11], v[10:11], v[4:5] op_sel_hi:[1,0]
	v_pk_mul_f32 v[12:13], v[12:13], v[4:5] op_sel_hi:[1,0]
	v_rcp_f32_e32 v28, v28
	v_pk_add_f32 v[186:187], v[186:187], v[2:3] op_sel:[0,1] op_sel_hi:[1,1]
	v_pk_add_f32 v[188:189], v[188:189], v[2:3] op_sel:[0,1] op_sel_hi:[1,1]
	v_med3_f32 v9, v9, s87, v227
	v_med3_f32 v10, v10, s87, v227
	v_med3_f32 v12, v12, s87, v227
	v_pk_mul_f32 v[14:15], v[14:15], v[202:203]
	v_rcp_f32_e32 v186, v186
	v_pk_add_f32 v[192:193], v[192:193], v[2:3] op_sel:[0,1] op_sel_hi:[1,1]
	v_pk_mul_f32 v[14:15], v[14:15], v[204:205]
	v_rcp_f32_e32 v188, v188
	v_cvt_pk_fp8_f32 v8, v8, v9
	v_pk_mul_f32 v[14:15], v[14:15], v[4:5] op_sel_hi:[1,0]
	v_med3_f32 v11, v11, s87, v227
	v_med3_f32 v13, v13, s87, v227
	v_med3_f32 v14, v14, s87, v227
	v_rcp_f32_e32 v192, v192
	v_cvt_pk_fp8_f32 v8, v10, v11 op_sel:[0,0,1]
	v_rcp_f32_e32 v29, v29
	v_cvt_pk_fp8_f32 v9, v12, v13
	v_med3_f32 v15, v15, s87, v227
	v_add_u32_e32 v10, 0x7e000, v241
	v_rcp_f32_e32 v187, v187
	v_cvt_pk_fp8_f32 v9, v14, v15 op_sel:[0,0,1]
	global_store_dwordx2 v10, v[6:7], s[26:27]
	v_rcp_f32_e32 v189, v189
	v_pk_mul_f32 v[6:7], v[42:43], v[250:251] op_sel:[0,1] op_sel_hi:[1,1]
	v_rcp_f32_e32 v193, v193
	v_pk_mul_f32 v[10:11], v[44:45], v[250:251] op_sel:[0,1] op_sel_hi:[1,1]
	v_pk_mul_f32 v[6:7], v[6:7], v[16:17]
	v_pk_mul_f32 v[12:13], v[34:35], v[250:251] op_sel:[0,1] op_sel_hi:[1,1]
	v_pk_mul_f32 v[10:11], v[10:11], v[30:31]
	v_pk_mul_f32 v[6:7], v[6:7], v[28:29]
	v_pk_mul_f32 v[12:13], v[12:13], v[32:33]
	v_pk_mul_f32 v[10:11], v[10:11], v[186:187]
	v_pk_mul_f32 v[6:7], v[6:7], v[4:5] op_sel_hi:[1,0]
	v_pk_mul_f32 v[12:13], v[12:13], v[188:189]
	v_pk_mul_f32 v[10:11], v[10:11], v[4:5] op_sel_hi:[1,0]
	v_med3_f32 v6, v6, s87, v227
	v_pk_mul_f32 v[12:13], v[12:13], v[4:5] op_sel_hi:[1,0]
	v_pk_mul_f32 v[14:15], v[36:37], v[250:251] op_sel:[0,1] op_sel_hi:[1,1]
	v_med3_f32 v7, v7, s87, v227
	v_med3_f32 v10, v10, s87, v227
	v_med3_f32 v12, v12, s87, v227
	v_pk_mul_f32 v[14:15], v[14:15], v[190:191]
	v_cvt_pk_fp8_f32 v6, v6, v7
	v_med3_f32 v11, v11, s87, v227
	v_pk_mul_f32 v[14:15], v[14:15], v[192:193]
	v_med3_f32 v13, v13, s87, v227
	v_cvt_pk_fp8_f32 v6, v10, v11 op_sel:[0,0,1]
	v_pk_mul_f32 v[14:15], v[14:15], v[4:5] op_sel_hi:[1,0]
	v_cvt_pk_fp8_f32 v7, v12, v13
	v_add_u32_e32 v10, 0x8c000, v241
	v_med3_f32 v14, v14, s87, v227
	v_add_u32_e32 v11, 0x9a000, v241
	global_store_dwordx2 v10, v[8:9], s[26:27]
	v_med3_f32 v15, v15, s87, v227
	v_cvt_pk_fp8_f32 v7, v14, v15 op_sel:[0,0,1]
	global_store_dwordx2 v11, v[6:7], s[26:27]
	s_andn2_b64 vcc, exec, s[44:45]
	s_mov_b64 s[44:45], -1
	s_cbranch_vccnz .LBB0_832
	s_andn2_b64 vcc, exec, s[30:31]
	s_cbranch_vccnz .LBB0_831
	s_barrier
	s_branch .LBB0_831

.LBB0_1693:
	s_add_i32 s91, s91, 2
	s_add_u32 s64, s70, 0x100
	s_addc_u32 s65, s71, 0
	s_and_b64 s[74:75], s[68:69], exec
	s_cselect_b32 s74, 0, s64
	s_cselect_b32 s75, 0, s65
	s_add_u32 s74, s28, s74
	s_addc_u32 s75, s29, s75
	s_add_u32 s92, s51, s70
	s_addc_u32 s93, s53, s71
	s_and_b64 s[68:69], s[68:69], exec
	s_cselect_b32 s69, s55, s93
	s_cselect_b32 s68, s54, s92
	s_add_i32 s93, 0, 0x10000
	s_add_i32 s92, 0, 0x14000
	v_add_u32_e32 v2, s93, v210
	v_add_u32_e32 v6, s92, v210
	ds_read_b128 v[26:29], v2
	ds_read_b128 v[30:33], v2 offset:1024
	ds_read_b128 v[18:21], v2 offset:2048
	ds_read_b128 v[22:25], v2 offset:3072
	ds_read_b128 v[10:13], v6
	ds_read_b128 v[14:17], v6 offset:1024
	ds_read_b128 v[2:5], v6 offset:2048
	ds_read_b128 v[6:9], v6 offset:3072
	v_lshl_add_u64 v[170:171], v[194:195], 0, s[70:71]
	s_add_i32 m0, s59, 0xc000
	ds_read_b128 v[196:199], v212
	ds_read_b128 v[200:203], v212 offset:1024
	ds_read_b128 v[214:217], v212 offset:2048
	ds_read_b128 v[218:221], v212 offset:3072
	ds_read_b128 v[236:239], v212 offset:4096
	ds_read_b128 v[240:243], v212 offset:5120
	ds_read_b128 v[244:247], v212 offset:6144
	ds_read_b128 v[248:251], v212 offset:7168
	global_load_lds_dwordx4 v[170:171], off
	v_lshl_add_u64 v[170:171], v[192:193], 0, s[70:71]
	s_add_i32 m0, s59, 0xe000
	s_nop 0
	global_load_lds_dwordx4 v[170:171], off
	s_waitcnt vmcnt(8)
	s_waitcnt lgkmcnt(0)
	s_barrier
	s_setprio 1
	s_waitcnt lgkmcnt(0)
	v_mfma_scale_f32_16x16x128_f8f6f4 v[154:157], v[26:33], v[196:203], v[154:157], v208, v207 op_sel_hi:[0,0,0]
	v_mfma_scale_f32_16x16x128_f8f6f4 v[150:153], v[18:25], v[196:203], v[150:153], v208, v207 op_sel_hi:[0,0,0]
	v_mfma_scale_f32_16x16x128_f8f6f4 v[142:145], v[26:33], v[214:221], v[142:145], v208, v207 op_sel_hi:[0,0,0]
	v_mfma_scale_f32_16x16x128_f8f6f4 v[134:137], v[18:25], v[214:221], v[134:137], v208, v207 op_sel_hi:[0,0,0]
	v_mfma_scale_f32_16x16x128_f8f6f4 v[126:129], v[26:33], v[236:243], v[126:129], v208, v207 op_sel_hi:[0,0,0]
	v_mfma_scale_f32_16x16x128_f8f6f4 v[118:121], v[18:25], v[236:243], v[118:121], v208, v207 op_sel_hi:[0,0,0]
	v_mfma_scale_f32_16x16x128_f8f6f4 v[110:113], v[26:33], v[244:251], v[110:113], v208, v207 op_sel_hi:[0,0,0]
	v_mfma_scale_f32_16x16x128_f8f6f4 v[102:105], v[18:25], v[244:251], v[102:105], v208, v207 op_sel_hi:[0,0,0]
	s_setprio 0
	s_setprio 1
	v_mfma_scale_f32_16x16x128_f8f6f4 v[158:161], v[10:17], v[196:203], v[158:161], v208, v207 op_sel_hi:[0,0,0]
	v_mfma_scale_f32_16x16x128_f8f6f4 v[146:149], v[2:9], v[196:203], v[146:149], v208, v207 op_sel_hi:[0,0,0]
	v_mfma_scale_f32_16x16x128_f8f6f4 v[138:141], v[10:17], v[214:221], v[138:141], v208, v207 op_sel_hi:[0,0,0]
	v_mfma_scale_f32_16x16x128_f8f6f4 v[130:133], v[2:9], v[214:221], v[130:133], v208, v207 op_sel_hi:[0,0,0]
	v_mfma_scale_f32_16x16x128_f8f6f4 v[122:125], v[10:17], v[236:243], v[122:125], v208, v207 op_sel_hi:[0,0,0]
	v_mfma_scale_f32_16x16x128_f8f6f4 v[114:117], v[2:9], v[236:243], v[114:117], v208, v207 op_sel_hi:[0,0,0]
	v_mfma_scale_f32_16x16x128_f8f6f4 v[106:109], v[10:17], v[244:251], v[106:109], v208, v207 op_sel_hi:[0,0,0]
	v_mfma_scale_f32_16x16x128_f8f6f4 v[98:101], v[2:9], v[244:251], v[98:101], v208, v207 op_sel_hi:[0,0,0]
	s_setprio 0
	s_barrier
	s_add_i32 s70, s93, s72
	v_lshl_add_u64 v[196:197], s[68:69], 0, v[162:163]
	s_mov_b32 m0, s70
	ds_read_b128 v[214:217], v212 offset:16384
	ds_read_b128 v[218:221], v212 offset:17408
	ds_read_b128 v[236:239], v212 offset:18432
	ds_read_b128 v[240:243], v212 offset:19456
	ds_read_b128 v[244:247], v212 offset:20480
	ds_read_b128 v[248:251], v212 offset:21504
	ds_read_b128 v[170:173], v212 offset:22528
	ds_read_b128 v[174:177], v212 offset:23552
	global_load_lds_dwordx4 v[196:197], off
	s_add_i32 m0, s70, 0x2000
	s_add_u32 s70, s68, 0x20000
	v_lshl_add_u64 v[198:199], s[68:69], 0, v[164:165]
	s_addc_u32 s71, s69, 0
	s_add_i32 s92, s92, s72
	global_load_lds_dwordx4 v[198:199], off
	v_mov_b32_e32 v179, v167
	v_lshl_add_u64 v[202:203], s[74:75], 0, v[166:167]
	v_lshl_add_u64 v[200:201], s[74:75], 0, v[178:179]
	s_waitcnt vmcnt(4)
	s_waitcnt lgkmcnt(0)
	s_barrier
	s_setprio 1
	s_waitcnt lgkmcnt(0)
	v_mfma_scale_f32_16x16x128_f8f6f4 v[94:97], v[26:33], v[214:221], v[94:97], v208, v207 op_sel_hi:[0,0,0]
	v_mfma_scale_f32_16x16x128_f8f6f4 v[86:89], v[18:25], v[214:221], v[86:89], v208, v207 op_sel_hi:[0,0,0]
	s_mov_b32 m0, s92
	v_mfma_scale_f32_16x16x128_f8f6f4 v[78:81], v[26:33], v[236:243], v[78:81], v208, v207 op_sel_hi:[0,0,0]
	global_load_lds_dwordx4 v162, s[70:71]
	v_mfma_scale_f32_16x16x128_f8f6f4 v[70:73], v[18:25], v[236:243], v[70:73], v208, v207 op_sel_hi:[0,0,0]
	v_mfma_scale_f32_16x16x128_f8f6f4 v[62:65], v[26:33], v[244:251], v[62:65], v208, v207 op_sel_hi:[0,0,0]
	s_add_i32 m0, s92, 0x2000
	v_mfma_scale_f32_16x16x128_f8f6f4 v[54:57], v[18:25], v[244:251], v[54:57], v208, v207 op_sel_hi:[0,0,0]
	global_load_lds_dwordx4 v164, s[70:71]
	v_mfma_scale_f32_16x16x128_f8f6f4 v[46:49], v[26:33], v[170:177], v[46:49], v208, v207 op_sel_hi:[0,0,0]
	v_mfma_scale_f32_16x16x128_f8f6f4 v[38:41], v[18:25], v[170:177], v[38:41], v208, v207 op_sel_hi:[0,0,0]
	s_setprio 0
	s_setprio 1
	v_mfma_scale_f32_16x16x128_f8f6f4 v[90:93], v[10:17], v[214:221], v[90:93], v208, v207 op_sel_hi:[0,0,0]
	s_mov_b32 m0, s59
	v_mfma_scale_f32_16x16x128_f8f6f4 v[82:85], v[2:9], v[214:221], v[82:85], v208, v207 op_sel_hi:[0,0,0]
	global_load_lds_dwordx4 v166, s[74:75]
	v_mfma_scale_f32_16x16x128_f8f6f4 v[74:77], v[10:17], v[236:243], v[74:77], v208, v207 op_sel_hi:[0,0,0]
	v_mfma_scale_f32_16x16x128_f8f6f4 v[66:69], v[2:9], v[236:243], v[66:69], v208, v207 op_sel_hi:[0,0,0]
	s_mov_b32 m0, s61
	v_mfma_scale_f32_16x16x128_f8f6f4 v[58:61], v[10:17], v[244:251], v[58:61], v208, v207 op_sel_hi:[0,0,0]
	global_load_lds_dwordx4 v178, s[74:75]
	v_mfma_scale_f32_16x16x128_f8f6f4 v[50:53], v[2:9], v[244:251], v[50:53], v208, v207 op_sel_hi:[0,0,0]
	v_mfma_scale_f32_16x16x128_f8f6f4 v[42:45], v[10:17], v[170:177], v[42:45], v208, v207 op_sel_hi:[0,0,0]
	v_mfma_scale_f32_16x16x128_f8f6f4 v[34:37], v[2:9], v[170:177], v[34:37], v208, v207 op_sel_hi:[0,0,0]
	s_setprio 0
	s_barrier
	s_add_i32 s70, 0, 0x18000
	s_add_i32 s71, 0, 0x1c000
	v_add_u32_e32 v2, s70, v210
	v_add_u32_e32 v6, s71, v210
	ds_read_b128 v[26:29], v2
	ds_read_b128 v[30:33], v2 offset:1024
	ds_read_b128 v[18:21], v2 offset:2048
	ds_read_b128 v[22:25], v2 offset:3072
	ds_read_b128 v[10:13], v6
	ds_read_b128 v[14:17], v6 offset:1024
	ds_read_b128 v[2:5], v6 offset:2048
	ds_read_b128 v[6:9], v6 offset:3072
	s_mov_b32 m0, s73
	ds_read_b128 v[170:173], v212 offset:32768
	ds_read_b128 v[174:177], v212 offset:33792
	ds_read_b128 v[214:217], v212 offset:34816
	ds_read_b128 v[218:221], v212 offset:35840
	ds_read_b128 v[236:239], v212 offset:36864
	ds_read_b128 v[240:243], v212 offset:37888
	ds_read_b128 v[244:247], v212 offset:38912
	ds_read_b128 v[248:251], v212 offset:39936
	global_load_lds_dwordx4 v180, s[74:75]
	s_mov_b32 m0, s76
	s_nop 0
	global_load_lds_dwordx4 v182, s[74:75]
	s_waitcnt vmcnt(8)
	s_waitcnt lgkmcnt(0)
	s_barrier
	s_setprio 1
	s_waitcnt lgkmcnt(0)
	v_mfma_scale_f32_16x16x128_f8f6f4 v[154:157], v[26:33], v[170:177], v[154:157], v208, v207 op_sel_hi:[0,0,0]
	v_mfma_scale_f32_16x16x128_f8f6f4 v[150:153], v[18:25], v[170:177], v[150:153], v208, v207 op_sel_hi:[0,0,0]
	v_mfma_scale_f32_16x16x128_f8f6f4 v[142:145], v[26:33], v[214:221], v[142:145], v208, v207 op_sel_hi:[0,0,0]
	v_mfma_scale_f32_16x16x128_f8f6f4 v[134:137], v[18:25], v[214:221], v[134:137], v208, v207 op_sel_hi:[0,0,0]
	v_mfma_scale_f32_16x16x128_f8f6f4 v[126:129], v[26:33], v[236:243], v[126:129], v208, v207 op_sel_hi:[0,0,0]
	v_mfma_scale_f32_16x16x128_f8f6f4 v[118:121], v[18:25], v[236:243], v[118:121], v208, v207 op_sel_hi:[0,0,0]
	v_mfma_scale_f32_16x16x128_f8f6f4 v[110:113], v[26:33], v[244:251], v[110:113], v208, v207 op_sel_hi:[0,0,0]
	v_mfma_scale_f32_16x16x128_f8f6f4 v[102:105], v[18:25], v[244:251], v[102:105], v208, v207 op_sel_hi:[0,0,0]
	s_setprio 0
	s_setprio 1
	v_mfma_scale_f32_16x16x128_f8f6f4 v[158:161], v[10:17], v[170:177], v[158:161], v208, v207 op_sel_hi:[0,0,0]
	v_mfma_scale_f32_16x16x128_f8f6f4 v[146:149], v[2:9], v[170:177], v[146:149], v208, v207 op_sel_hi:[0,0,0]
	v_mfma_scale_f32_16x16x128_f8f6f4 v[138:141], v[10:17], v[214:221], v[138:141], v208, v207 op_sel_hi:[0,0,0]
	v_mfma_scale_f32_16x16x128_f8f6f4 v[130:133], v[2:9], v[214:221], v[130:133], v208, v207 op_sel_hi:[0,0,0]
	v_mfma_scale_f32_16x16x128_f8f6f4 v[122:125], v[10:17], v[236:243], v[122:125], v208, v207 op_sel_hi:[0,0,0]
	v_mfma_scale_f32_16x16x128_f8f6f4 v[114:117], v[2:9], v[236:243], v[114:117], v208, v207 op_sel_hi:[0,0,0]
	v_mfma_scale_f32_16x16x128_f8f6f4 v[106:109], v[10:17], v[244:251], v[106:109], v208, v207 op_sel_hi:[0,0,0]
	v_mfma_scale_f32_16x16x128_f8f6f4 v[98:101], v[2:9], v[244:251], v[98:101], v208, v207 op_sel_hi:[0,0,0]
	s_setprio 0
	s_barrier
	s_add_i32 s70, s70, s72
	v_lshl_add_u64 v[196:197], v[196:197], 0, s[56:57]
	s_mov_b32 m0, s70
	ds_read_b128 v[170:173], v212 offset:49152
	ds_read_b128 v[174:177], v212 offset:50176
	ds_read_b128 v[214:217], v212 offset:51200
	ds_read_b128 v[218:221], v212 offset:52224
	ds_read_b128 v[236:239], v212 offset:53248
	ds_read_b128 v[240:243], v212 offset:54272
	ds_read_b128 v[244:247], v212 offset:55296
	ds_read_b128 v[248:251], v212 offset:56320
	global_load_lds_dwordx4 v[196:197], off
	s_add_i32 m0, s70, 0x2000
	s_add_u32 s68, s68, 0x20080
	v_lshl_add_u64 v[196:197], v[198:199], 0, s[56:57]
	s_addc_u32 s69, s69, 0
	s_add_i32 s70, s71, s72
	global_load_lds_dwordx4 v[196:197], off
	s_waitcnt vmcnt(4)
	s_waitcnt lgkmcnt(0)
	s_barrier
	s_setprio 1
	s_waitcnt lgkmcnt(0)
	v_mfma_scale_f32_16x16x128_f8f6f4 v[94:97], v[26:33], v[170:177], v[94:97], v208, v207 op_sel_hi:[0,0,0]
	v_mfma_scale_f32_16x16x128_f8f6f4 v[86:89], v[18:25], v[170:177], v[86:89], v208, v207 op_sel_hi:[0,0,0]
	s_mov_b32 m0, s70
	v_mfma_scale_f32_16x16x128_f8f6f4 v[78:81], v[26:33], v[214:221], v[78:81], v208, v207 op_sel_hi:[0,0,0]
	global_load_lds_dwordx4 v162, s[68:69]
	v_mfma_scale_f32_16x16x128_f8f6f4 v[70:73], v[18:25], v[214:221], v[70:73], v208, v207 op_sel_hi:[0,0,0]
	v_mfma_scale_f32_16x16x128_f8f6f4 v[62:65], v[26:33], v[236:243], v[62:65], v208, v207 op_sel_hi:[0,0,0]
	s_add_i32 m0, s70, 0x2000
	v_mfma_scale_f32_16x16x128_f8f6f4 v[54:57], v[18:25], v[236:243], v[54:57], v208, v207 op_sel_hi:[0,0,0]
	global_load_lds_dwordx4 v164, s[68:69]
	v_mfma_scale_f32_16x16x128_f8f6f4 v[46:49], v[26:33], v[244:251], v[46:49], v208, v207 op_sel_hi:[0,0,0]
	v_mfma_scale_f32_16x16x128_f8f6f4 v[38:41], v[18:25], v[244:251], v[38:41], v208, v207 op_sel_hi:[0,0,0]
	s_setprio 0
	s_setprio 1
	v_mfma_scale_f32_16x16x128_f8f6f4 v[90:93], v[10:17], v[170:177], v[90:93], v208, v207 op_sel_hi:[0,0,0]
	s_add_i32 m0, s77, 0xffffff80
	v_mfma_scale_f32_16x16x128_f8f6f4 v[82:85], v[2:9], v[170:177], v[82:85], v208, v207 op_sel_hi:[0,0,0]
	global_load_lds_dwordx4 v166, s[74:75] offset:128
	v_mfma_scale_f32_16x16x128_f8f6f4 v[74:77], v[10:17], v[214:221], v[74:77], v208, v207 op_sel_hi:[0,0,0]
	v_mfma_scale_f32_16x16x128_f8f6f4 v[66:69], v[2:9], v[214:221], v[66:69], v208, v207 op_sel_hi:[0,0,0]
	s_add_i32 m0, s79, 0xffffff80
	v_mfma_scale_f32_16x16x128_f8f6f4 v[58:61], v[10:17], v[236:243], v[58:61], v208, v207 op_sel_hi:[0,0,0]
	global_load_lds_dwordx4 v178, s[74:75] offset:128
	v_mfma_scale_f32_16x16x128_f8f6f4 v[50:53], v[2:9], v[236:243], v[50:53], v208, v207 op_sel_hi:[0,0,0]
	v_mfma_scale_f32_16x16x128_f8f6f4 v[42:45], v[10:17], v[244:251], v[42:45], v208, v207 op_sel_hi:[0,0,0]
	v_mfma_scale_f32_16x16x128_f8f6f4 v[34:37], v[2:9], v[244:251], v[34:37], v208, v207 op_sel_hi:[0,0,0]
	s_setprio 0
	s_barrier
	s_cmp_ge_i32 s91, s11
	s_cbranch_scc1 .LBB0_1695
	s_mov_b64 s[70:71], s[64:65]
	s_branch .LBB0_1691

.LBB0_1838:
	s_add_i32 s55, s55, 2
	s_add_u32 s60, s64, 0x100
	s_addc_u32 s61, s65, 0
	s_and_b64 s[68:69], s[62:63], exec
	s_cselect_b32 s68, 0, s60
	s_cselect_b32 s69, 0, s61
	s_add_u32 s68, s30, s68
	s_addc_u32 s69, s31, s69
	s_add_u32 s91, s47, s64
	s_addc_u32 s92, s49, s65
	s_and_b64 s[62:63], s[62:63], exec
	s_cselect_b32 s63, s53, s92
	s_cselect_b32 s62, s52, s91
	s_add_i32 s92, 0, 0x10000
	s_add_i32 s91, 0, 0x14000
	v_add_u32_e32 v2, s92, v210
	v_add_u32_e32 v6, s91, v210
	ds_read_b128 v[26:29], v2
	ds_read_b128 v[30:33], v2 offset:1024
	ds_read_b128 v[18:21], v2 offset:2048
	ds_read_b128 v[22:25], v2 offset:3072
	ds_read_b128 v[10:13], v6
	ds_read_b128 v[14:17], v6 offset:1024
	ds_read_b128 v[2:5], v6 offset:2048
	ds_read_b128 v[6:9], v6 offset:3072
	v_lshl_add_u64 v[222:223], v[194:195], 0, s[64:65]
	s_add_i32 m0, s59, 0xc000
	ds_read_b128 v[170:173], v212
	ds_read_b128 v[174:177], v212 offset:1024
	ds_read_b128 v[196:199], v212 offset:2048
	ds_read_b128 v[200:203], v212 offset:3072
	ds_read_b128 v[214:217], v212 offset:4096
	ds_read_b128 v[218:221], v212 offset:5120
	ds_read_b128 v[236:239], v212 offset:6144
	ds_read_b128 v[240:243], v212 offset:7168
	global_load_lds_dwordx4 v[222:223], off
	v_lshl_add_u64 v[222:223], v[192:193], 0, s[64:65]
	s_add_i32 m0, s59, 0xe000
	s_nop 0
	global_load_lds_dwordx4 v[222:223], off
	s_waitcnt vmcnt(8)
	s_waitcnt lgkmcnt(0)
	s_barrier
	s_setprio 1
	s_waitcnt lgkmcnt(0)
	v_mfma_scale_f32_16x16x128_f8f6f4 v[154:157], v[26:33], v[170:177], v[154:157], v208, v207 op_sel_hi:[0,0,0]
	v_mfma_scale_f32_16x16x128_f8f6f4 v[150:153], v[18:25], v[170:177], v[150:153], v208, v207 op_sel_hi:[0,0,0]
	v_mfma_scale_f32_16x16x128_f8f6f4 v[142:145], v[26:33], v[196:203], v[142:145], v208, v207 op_sel_hi:[0,0,0]
	v_mfma_scale_f32_16x16x128_f8f6f4 v[134:137], v[18:25], v[196:203], v[134:137], v208, v207 op_sel_hi:[0,0,0]
	v_mfma_scale_f32_16x16x128_f8f6f4 v[126:129], v[26:33], v[214:221], v[126:129], v208, v207 op_sel_hi:[0,0,0]
	v_mfma_scale_f32_16x16x128_f8f6f4 v[118:121], v[18:25], v[214:221], v[118:121], v208, v207 op_sel_hi:[0,0,0]
	v_mfma_scale_f32_16x16x128_f8f6f4 v[110:113], v[26:33], v[236:243], v[110:113], v208, v207 op_sel_hi:[0,0,0]
	v_mfma_scale_f32_16x16x128_f8f6f4 v[102:105], v[18:25], v[236:243], v[102:105], v208, v207 op_sel_hi:[0,0,0]
	s_setprio 0
	s_setprio 1
	v_mfma_scale_f32_16x16x128_f8f6f4 v[158:161], v[10:17], v[170:177], v[158:161], v208, v207 op_sel_hi:[0,0,0]
	v_mfma_scale_f32_16x16x128_f8f6f4 v[146:149], v[2:9], v[170:177], v[146:149], v208, v207 op_sel_hi:[0,0,0]
	v_mfma_scale_f32_16x16x128_f8f6f4 v[138:141], v[10:17], v[196:203], v[138:141], v208, v207 op_sel_hi:[0,0,0]
	v_mfma_scale_f32_16x16x128_f8f6f4 v[130:133], v[2:9], v[196:203], v[130:133], v208, v207 op_sel_hi:[0,0,0]
	v_mfma_scale_f32_16x16x128_f8f6f4 v[122:125], v[10:17], v[214:221], v[122:125], v208, v207 op_sel_hi:[0,0,0]
	v_mfma_scale_f32_16x16x128_f8f6f4 v[114:117], v[2:9], v[214:221], v[114:117], v208, v207 op_sel_hi:[0,0,0]
	v_mfma_scale_f32_16x16x128_f8f6f4 v[106:109], v[10:17], v[236:243], v[106:109], v208, v207 op_sel_hi:[0,0,0]
	v_mfma_scale_f32_16x16x128_f8f6f4 v[98:101], v[2:9], v[236:243], v[98:101], v208, v207 op_sel_hi:[0,0,0]
	s_setprio 0
	s_barrier
	s_add_i32 s64, s92, s22
	v_lshl_add_u64 v[196:197], s[62:63], 0, v[162:163]
	s_mov_b32 m0, s64
	ds_read_b128 v[170:173], v212 offset:16384
	ds_read_b128 v[174:177], v212 offset:17408
	ds_read_b128 v[214:217], v212 offset:18432
	ds_read_b128 v[218:221], v212 offset:19456
	ds_read_b128 v[236:239], v212 offset:20480
	ds_read_b128 v[240:243], v212 offset:21504
	ds_read_b128 v[244:247], v212 offset:22528
	ds_read_b128 v[248:251], v212 offset:23552
	global_load_lds_dwordx4 v[196:197], off
	s_add_i32 m0, s64, 0x2000
	s_add_u32 s64, s62, 0x20000
	v_lshl_add_u64 v[198:199], s[62:63], 0, v[164:165]
	s_addc_u32 s65, s63, 0
	s_add_i32 s91, s91, s22
	global_load_lds_dwordx4 v[198:199], off
	v_mov_b32_e32 v179, v167
	v_lshl_add_u64 v[202:203], s[68:69], 0, v[166:167]
	v_lshl_add_u64 v[200:201], s[68:69], 0, v[178:179]
	s_waitcnt vmcnt(4)
	s_waitcnt lgkmcnt(0)
	s_barrier
	s_setprio 1
	s_waitcnt lgkmcnt(0)
	v_mfma_scale_f32_16x16x128_f8f6f4 v[94:97], v[26:33], v[170:177], v[94:97], v208, v207 op_sel_hi:[0,0,0]
	v_mfma_scale_f32_16x16x128_f8f6f4 v[86:89], v[18:25], v[170:177], v[86:89], v208, v207 op_sel_hi:[0,0,0]
	s_mov_b32 m0, s91
	v_mfma_scale_f32_16x16x128_f8f6f4 v[78:81], v[26:33], v[214:221], v[78:81], v208, v207 op_sel_hi:[0,0,0]
	global_load_lds_dwordx4 v162, s[64:65]
	v_mfma_scale_f32_16x16x128_f8f6f4 v[70:73], v[18:25], v[214:221], v[70:73], v208, v207 op_sel_hi:[0,0,0]
	v_mfma_scale_f32_16x16x128_f8f6f4 v[62:65], v[26:33], v[236:243], v[62:65], v208, v207 op_sel_hi:[0,0,0]
	s_add_i32 m0, s91, 0x2000
	v_mfma_scale_f32_16x16x128_f8f6f4 v[54:57], v[18:25], v[236:243], v[54:57], v208, v207 op_sel_hi:[0,0,0]
	global_load_lds_dwordx4 v164, s[64:65]
	v_mfma_scale_f32_16x16x128_f8f6f4 v[46:49], v[26:33], v[244:251], v[46:49], v208, v207 op_sel_hi:[0,0,0]
	v_mfma_scale_f32_16x16x128_f8f6f4 v[38:41], v[18:25], v[244:251], v[38:41], v208, v207 op_sel_hi:[0,0,0]
	s_setprio 0
	s_setprio 1
	v_mfma_scale_f32_16x16x128_f8f6f4 v[90:93], v[10:17], v[170:177], v[90:93], v208, v207 op_sel_hi:[0,0,0]
	s_mov_b32 m0, s59
	v_mfma_scale_f32_16x16x128_f8f6f4 v[82:85], v[2:9], v[170:177], v[82:85], v208, v207 op_sel_hi:[0,0,0]
	global_load_lds_dwordx4 v166, s[68:69]
	v_mfma_scale_f32_16x16x128_f8f6f4 v[74:77], v[10:17], v[214:221], v[74:77], v208, v207 op_sel_hi:[0,0,0]
	v_mfma_scale_f32_16x16x128_f8f6f4 v[66:69], v[2:9], v[214:221], v[66:69], v208, v207 op_sel_hi:[0,0,0]
	s_mov_b32 m0, s71
	v_mfma_scale_f32_16x16x128_f8f6f4 v[58:61], v[10:17], v[236:243], v[58:61], v208, v207 op_sel_hi:[0,0,0]
	global_load_lds_dwordx4 v178, s[68:69]
	v_mfma_scale_f32_16x16x128_f8f6f4 v[50:53], v[2:9], v[236:243], v[50:53], v208, v207 op_sel_hi:[0,0,0]
	v_mfma_scale_f32_16x16x128_f8f6f4 v[42:45], v[10:17], v[244:251], v[42:45], v208, v207 op_sel_hi:[0,0,0]
	v_mfma_scale_f32_16x16x128_f8f6f4 v[34:37], v[2:9], v[244:251], v[34:37], v208, v207 op_sel_hi:[0,0,0]
	s_setprio 0
	s_barrier
	s_add_i32 s64, 0, 0x18000
	s_add_i32 s65, 0, 0x1c000
	v_add_u32_e32 v2, s64, v210
	v_add_u32_e32 v6, s65, v210
	ds_read_b128 v[26:29], v2
	ds_read_b128 v[30:33], v2 offset:1024
	ds_read_b128 v[18:21], v2 offset:2048
	ds_read_b128 v[22:25], v2 offset:3072
	ds_read_b128 v[10:13], v6
	ds_read_b128 v[14:17], v6 offset:1024
	ds_read_b128 v[2:5], v6 offset:2048
	ds_read_b128 v[6:9], v6 offset:3072
	s_mov_b32 m0, s72
	ds_read_b128 v[170:173], v212 offset:32768
	ds_read_b128 v[174:177], v212 offset:33792
	ds_read_b128 v[214:217], v212 offset:34816
	ds_read_b128 v[218:221], v212 offset:35840
	ds_read_b128 v[236:239], v212 offset:36864
	ds_read_b128 v[240:243], v212 offset:37888
	ds_read_b128 v[244:247], v212 offset:38912
	ds_read_b128 v[248:251], v212 offset:39936
	global_load_lds_dwordx4 v180, s[68:69]
	s_mov_b32 m0, s73
	s_nop 0
	global_load_lds_dwordx4 v182, s[68:69]
	s_waitcnt vmcnt(8)
	s_waitcnt lgkmcnt(0)
	s_barrier
	s_setprio 1
	s_waitcnt lgkmcnt(0)
	v_mfma_scale_f32_16x16x128_f8f6f4 v[154:157], v[26:33], v[170:177], v[154:157], v208, v207 op_sel_hi:[0,0,0]
	v_mfma_scale_f32_16x16x128_f8f6f4 v[150:153], v[18:25], v[170:177], v[150:153], v208, v207 op_sel_hi:[0,0,0]
	v_mfma_scale_f32_16x16x128_f8f6f4 v[142:145], v[26:33], v[214:221], v[142:145], v208, v207 op_sel_hi:[0,0,0]
	v_mfma_scale_f32_16x16x128_f8f6f4 v[134:137], v[18:25], v[214:221], v[134:137], v208, v207 op_sel_hi:[0,0,0]
	v_mfma_scale_f32_16x16x128_f8f6f4 v[126:129], v[26:33], v[236:243], v[126:129], v208, v207 op_sel_hi:[0,0,0]
	v_mfma_scale_f32_16x16x128_f8f6f4 v[118:121], v[18:25], v[236:243], v[118:121], v208, v207 op_sel_hi:[0,0,0]
	v_mfma_scale_f32_16x16x128_f8f6f4 v[110:113], v[26:33], v[244:251], v[110:113], v208, v207 op_sel_hi:[0,0,0]
	v_mfma_scale_f32_16x16x128_f8f6f4 v[102:105], v[18:25], v[244:251], v[102:105], v208, v207 op_sel_hi:[0,0,0]
	s_setprio 0
	s_setprio 1
	v_mfma_scale_f32_16x16x128_f8f6f4 v[158:161], v[10:17], v[170:177], v[158:161], v208, v207 op_sel_hi:[0,0,0]
	v_mfma_scale_f32_16x16x128_f8f6f4 v[146:149], v[2:9], v[170:177], v[146:149], v208, v207 op_sel_hi:[0,0,0]
	v_mfma_scale_f32_16x16x128_f8f6f4 v[138:141], v[10:17], v[214:221], v[138:141], v208, v207 op_sel_hi:[0,0,0]
	v_mfma_scale_f32_16x16x128_f8f6f4 v[130:133], v[2:9], v[214:221], v[130:133], v208, v207 op_sel_hi:[0,0,0]
	v_mfma_scale_f32_16x16x128_f8f6f4 v[122:125], v[10:17], v[236:243], v[122:125], v208, v207 op_sel_hi:[0,0,0]
	v_mfma_scale_f32_16x16x128_f8f6f4 v[114:117], v[2:9], v[236:243], v[114:117], v208, v207 op_sel_hi:[0,0,0]
	v_mfma_scale_f32_16x16x128_f8f6f4 v[106:109], v[10:17], v[244:251], v[106:109], v208, v207 op_sel_hi:[0,0,0]
	v_mfma_scale_f32_16x16x128_f8f6f4 v[98:101], v[2:9], v[244:251], v[98:101], v208, v207 op_sel_hi:[0,0,0]
	s_setprio 0
	s_barrier
	s_add_i32 s64, s64, s22
	v_lshl_add_u64 v[196:197], v[196:197], 0, s[56:57]
	s_mov_b32 m0, s64
	ds_read_b128 v[170:173], v212 offset:49152
	ds_read_b128 v[174:177], v212 offset:50176
	ds_read_b128 v[214:217], v212 offset:51200
	ds_read_b128 v[218:221], v212 offset:52224
	ds_read_b128 v[236:239], v212 offset:53248
	ds_read_b128 v[240:243], v212 offset:54272
	ds_read_b128 v[244:247], v212 offset:55296
	ds_read_b128 v[248:251], v212 offset:56320
	global_load_lds_dwordx4 v[196:197], off
	s_add_i32 m0, s64, 0x2000
	s_add_u32 s62, s62, 0x20080
	v_lshl_add_u64 v[196:197], v[198:199], 0, s[56:57]
	s_addc_u32 s63, s63, 0
	s_add_i32 s64, s65, s22
	global_load_lds_dwordx4 v[196:197], off
	s_waitcnt vmcnt(4)
	s_waitcnt lgkmcnt(0)
	s_barrier
	s_setprio 1
	s_waitcnt lgkmcnt(0)
	v_mfma_scale_f32_16x16x128_f8f6f4 v[94:97], v[26:33], v[170:177], v[94:97], v208, v207 op_sel_hi:[0,0,0]
	v_mfma_scale_f32_16x16x128_f8f6f4 v[86:89], v[18:25], v[170:177], v[86:89], v208, v207 op_sel_hi:[0,0,0]
	s_mov_b32 m0, s64
	v_mfma_scale_f32_16x16x128_f8f6f4 v[78:81], v[26:33], v[214:221], v[78:81], v208, v207 op_sel_hi:[0,0,0]
	global_load_lds_dwordx4 v162, s[62:63]
	v_mfma_scale_f32_16x16x128_f8f6f4 v[70:73], v[18:25], v[214:221], v[70:73], v208, v207 op_sel_hi:[0,0,0]
	v_mfma_scale_f32_16x16x128_f8f6f4 v[62:65], v[26:33], v[236:243], v[62:65], v208, v207 op_sel_hi:[0,0,0]
	s_add_i32 m0, s64, 0x2000
	v_mfma_scale_f32_16x16x128_f8f6f4 v[54:57], v[18:25], v[236:243], v[54:57], v208, v207 op_sel_hi:[0,0,0]
	global_load_lds_dwordx4 v164, s[62:63]
	v_mfma_scale_f32_16x16x128_f8f6f4 v[46:49], v[26:33], v[244:251], v[46:49], v208, v207 op_sel_hi:[0,0,0]
	v_mfma_scale_f32_16x16x128_f8f6f4 v[38:41], v[18:25], v[244:251], v[38:41], v208, v207 op_sel_hi:[0,0,0]
	s_setprio 0
	s_setprio 1
	v_mfma_scale_f32_16x16x128_f8f6f4 v[90:93], v[10:17], v[170:177], v[90:93], v208, v207 op_sel_hi:[0,0,0]
	s_add_i32 m0, s74, 0xffffff80
	v_mfma_scale_f32_16x16x128_f8f6f4 v[82:85], v[2:9], v[170:177], v[82:85], v208, v207 op_sel_hi:[0,0,0]
	global_load_lds_dwordx4 v166, s[68:69] offset:128
	v_mfma_scale_f32_16x16x128_f8f6f4 v[74:77], v[10:17], v[214:221], v[74:77], v208, v207 op_sel_hi:[0,0,0]
	v_mfma_scale_f32_16x16x128_f8f6f4 v[66:69], v[2:9], v[214:221], v[66:69], v208, v207 op_sel_hi:[0,0,0]
	s_add_i32 m0, s75, 0xffffff80
	v_mfma_scale_f32_16x16x128_f8f6f4 v[58:61], v[10:17], v[236:243], v[58:61], v208, v207 op_sel_hi:[0,0,0]
	global_load_lds_dwordx4 v178, s[68:69] offset:128
	v_mfma_scale_f32_16x16x128_f8f6f4 v[50:53], v[2:9], v[236:243], v[50:53], v208, v207 op_sel_hi:[0,0,0]
	v_mfma_scale_f32_16x16x128_f8f6f4 v[42:45], v[10:17], v[244:251], v[42:45], v208, v207 op_sel_hi:[0,0,0]
	v_mfma_scale_f32_16x16x128_f8f6f4 v[34:37], v[2:9], v[244:251], v[34:37], v208, v207 op_sel_hi:[0,0,0]
	s_setprio 0
	s_barrier
	s_cmp_lt_i32 s55, s11
	s_cbranch_scc0 .LBB0_1841
	s_mov_b64 s[64:65], s[60:61]
	s_branch .LBB0_1836
